# expert-weight conversion source loads plain (no nt)
# baseline (speedup 1.0000x reference)
.LBB0_465:
	s_or_b64 exec, exec, s[4:5]
	s_waitcnt lgkmcnt(0)
	s_barrier
	ds_read_b32 v4, v12
	s_mov_b64 s[4:5], -1
	s_waitcnt lgkmcnt(0)
	v_cmp_lt_u32_e32 vcc, s16, v4
	v_readfirstlane_b32 s2, v4
	s_cbranch_vccnz .LBB0_458
	s_lshl_b32 s6, s2, 3
	s_add_i32 s6, s6, s91
	s_cmpk_gt_u32 s6, 0x5fff
	s_cbranch_scc1 .LBB0_457
	s_lshl_b32 s7, s6, 5
	s_cmpk_gt_u32 s6, 0x3fff
	s_cbranch_scc0 .LBB0_469
	s_add_i32 s2, s6, 0xffffc000
	s_lshr_b32 s2, s2, 8
	s_lshl_b64 s[4:5], s[2:3], 20
	s_lshl_b64 s[8:9], s[2:3], 22
	s_add_u32 s8, s76, s8
	s_addc_u32 s9, s77, s9
	s_add_u32 s4, s10, s4
	s_addc_u32 s5, s11, s5
	s_lshl_b32 s2, s6, 2
	s_and_b32 s44, s2, 0x380
	s_and_b32 s2, s7, 0x3e0
	v_or_b32_e32 v4, s2, v6
	v_or_b32_e32 v42, s44, v7
	v_lshlrev_b32_e32 v4, 2, v4
	v_lshl_add_u64 v[40:41], s[8:9], 0, v[4:5]
	v_lshlrev_b32_e32 v4, 12, v42
	v_lshl_add_u64 v[96:97], v[40:41], 0, v[4:5]
	v_add_co_u32_e32 v44, vcc, s17, v96
	global_load_dwordx4 v[40:43], v[96:97], off
	s_nop 0
	v_addc_co_u32_e32 v45, vcc, 0, v97, vcc
	global_load_dwordx4 v[44:47], v[44:45], off
	v_add_co_u32_e32 v48, vcc, s18, v96
	s_add_u32 s4, s4, s44
	s_nop 0
	v_addc_co_u32_e32 v49, vcc, 0, v97, vcc
	v_add_co_u32_e32 v52, vcc, s19, v96
	global_load_dwordx4 v[48:51], v[48:49], off
	s_nop 0
	v_addc_co_u32_e32 v53, vcc, 0, v97, vcc
	global_load_dwordx4 v[52:55], v[52:53], off
	v_add_co_u32_e32 v56, vcc, s20, v96
	s_addc_u32 s5, s5, 0
	s_nop 0
	v_addc_co_u32_e32 v57, vcc, 0, v97, vcc
	v_add_co_u32_e32 v60, vcc, s21, v96
	global_load_dwordx4 v[56:59], v[56:57], off
	s_nop 0
	v_addc_co_u32_e32 v61, vcc, 0, v97, vcc
	global_load_dwordx4 v[60:63], v[60:61], off
	v_add_co_u32_e32 v64, vcc, s22, v96
	s_nop 1
	v_addc_co_u32_e32 v65, vcc, 0, v97, vcc
	v_add_co_u32_e32 v68, vcc, s23, v96
	global_load_dwordx4 v[64:67], v[64:65], off
	s_nop 0
	v_addc_co_u32_e32 v69, vcc, 0, v97, vcc
	global_load_dwordx4 v[68:71], v[68:69], off
	v_add_co_u32_e32 v72, vcc, s24, v96
	s_waitcnt vmcnt(7)
	v_mul_f32_e32 v4, 0x42800000, v40
	v_addc_co_u32_e32 v73, vcc, 0, v97, vcc
	v_add_co_u32_e32 v76, vcc, s25, v96
	v_mul_f32_e32 v40, 0x42800000, v41
	s_nop 0
	v_addc_co_u32_e32 v77, vcc, 0, v97, vcc
	global_load_dwordx4 v[72:75], v[72:73], off
	s_nop 0
	global_load_dwordx4 v[76:79], v[76:77], off
	v_add_co_u32_e32 v80, vcc, s26, v96
	v_mul_f32_e32 v41, 0x42800000, v42
	s_nop 0
	v_addc_co_u32_e32 v81, vcc, 0, v97, vcc
	v_add_co_u32_e32 v84, vcc, s27, v96
	v_mul_f32_e32 v42, 0x42800000, v43
	s_nop 0
	v_addc_co_u32_e32 v85, vcc, 0, v97, vcc
	global_load_dwordx4 v[80:83], v[80:81], off
	s_nop 0
	global_load_dwordx4 v[84:87], v[84:85], off
	v_add_co_u32_e32 v88, vcc, s28, v96
	s_waitcnt vmcnt(10)
	v_mul_f32_e32 v43, 0x42800000, v44
	v_addc_co_u32_e32 v89, vcc, 0, v97, vcc
	v_add_co_u32_e32 v92, vcc, s29, v96
	s_nop 1
	v_addc_co_u32_e32 v93, vcc, 0, v97, vcc
	global_load_dwordx4 v[88:91], v[88:89], off
	s_nop 0
	global_load_dwordx4 v[92:95], v[92:93], off
	v_add_co_u32_e32 v98, vcc, s30, v96
	s_nop 1
	v_addc_co_u32_e32 v99, vcc, 0, v97, vcc
	v_add_co_u32_e32 v100, vcc, s31, v96
	s_nop 1
	v_addc_co_u32_e32 v101, vcc, 0, v97, vcc
	global_load_dwordx4 v[96:99], v[98:99], off
	s_nop 0
	global_load_dwordx4 v[100:103], v[100:101], off
	ds_write2_b32 v8, v4, v43 offset1:8
	v_mul_f32_e32 v4, 0x42800000, v45
	ds_write2_b32 v8, v40, v4 offset0:129 offset1:137
	v_mul_f32_e32 v4, 0x42800000, v46
	ds_write2_b32 v38, v41, v4 offset0:2 offset1:10
	v_mul_f32_e32 v4, 0x42800000, v47
	ds_write2_b32 v38, v42, v4 offset0:131 offset1:139
	s_waitcnt vmcnt(13)
	v_mul_f32_e32 v4, 0x42800000, v48
	s_waitcnt vmcnt(12)
	v_mul_f32_e32 v43, 0x42800000, v52
	v_mul_f32_e32 v40, 0x42800000, v49
	ds_write2_b32 v8, v4, v43 offset0:16 offset1:24
	v_mul_f32_e32 v4, 0x42800000, v53
	v_mul_f32_e32 v41, 0x42800000, v50
	ds_write2_b32 v8, v40, v4 offset0:145 offset1:153
	v_mul_f32_e32 v4, 0x42800000, v54
	v_mul_f32_e32 v42, 0x42800000, v51
	ds_write2_b32 v38, v41, v4 offset0:18 offset1:26
	v_mul_f32_e32 v4, 0x42800000, v55
	ds_write2_b32 v38, v42, v4 offset0:147 offset1:155
	s_waitcnt vmcnt(11)
	v_mul_f32_e32 v4, 0x42800000, v56
	s_waitcnt vmcnt(10)
	v_mul_f32_e32 v43, 0x42800000, v60
	v_mul_f32_e32 v40, 0x42800000, v57
	ds_write2_b32 v8, v4, v43 offset0:32 offset1:40
	v_mul_f32_e32 v4, 0x42800000, v61
	v_mul_f32_e32 v41, 0x42800000, v58
	ds_write2_b32 v8, v40, v4 offset0:161 offset1:169
	v_mul_f32_e32 v4, 0x42800000, v62
	v_mul_f32_e32 v42, 0x42800000, v59
	ds_write2_b32 v38, v41, v4 offset0:34 offset1:42
	v_mul_f32_e32 v4, 0x42800000, v63
	ds_write2_b32 v38, v42, v4 offset0:163 offset1:171
	s_waitcnt vmcnt(9)
	v_mul_f32_e32 v4, 0x42800000, v64
	s_waitcnt vmcnt(8)
	v_mul_f32_e32 v43, 0x42800000, v68
	v_mul_f32_e32 v40, 0x42800000, v65
	ds_write2_b32 v8, v4, v43 offset0:48 offset1:56
	v_mul_f32_e32 v4, 0x42800000, v69
	v_mul_f32_e32 v41, 0x42800000, v66
	ds_write2_b32 v8, v40, v4 offset0:177 offset1:185
	v_mul_f32_e32 v4, 0x42800000, v70
	v_mul_f32_e32 v42, 0x42800000, v67
	ds_write2_b32 v38, v41, v4 offset0:50 offset1:58
	v_mul_f32_e32 v4, 0x42800000, v71
	ds_write2_b32 v38, v42, v4 offset0:179 offset1:187
	v_lshl_add_u64 v[48:49], s[4:5], 0, v[2:3]
	s_mov_b64 s[4:5], 0
	s_waitcnt vmcnt(7)
	v_mul_f32_e32 v4, 0x42800000, v72
	s_waitcnt vmcnt(6)
	v_mul_f32_e32 v43, 0x42800000, v76
	v_mul_f32_e32 v40, 0x42800000, v73
	ds_write2_b32 v8, v4, v43 offset0:64 offset1:72
	v_mul_f32_e32 v4, 0x42800000, v77
	v_mul_f32_e32 v41, 0x42800000, v74
	ds_write2_b32 v8, v40, v4 offset0:193 offset1:201
	v_mul_f32_e32 v4, 0x42800000, v78
	v_mul_f32_e32 v42, 0x42800000, v75
	ds_write2_b32 v38, v41, v4 offset0:66 offset1:74
	v_mul_f32_e32 v4, 0x42800000, v79
	ds_write2_b32 v38, v42, v4 offset0:195 offset1:203
	s_waitcnt vmcnt(5)
	v_mul_f32_e32 v4, 0x42800000, v80
	s_waitcnt vmcnt(4)
	v_mul_f32_e32 v43, 0x42800000, v84
	v_mul_f32_e32 v40, 0x42800000, v81
	ds_write2_b32 v8, v4, v43 offset0:80 offset1:88
	v_mul_f32_e32 v4, 0x42800000, v85
	v_mul_f32_e32 v41, 0x42800000, v82
	ds_write2_b32 v8, v40, v4 offset0:209 offset1:217
	v_mul_f32_e32 v4, 0x42800000, v86
	v_mul_f32_e32 v42, 0x42800000, v83
	ds_write2_b32 v38, v41, v4 offset0:82 offset1:90
	v_mul_f32_e32 v4, 0x42800000, v87
	ds_write2_b32 v38, v42, v4 offset0:211 offset1:219
	s_waitcnt vmcnt(3)
	v_mul_f32_e32 v4, 0x42800000, v88
	s_waitcnt vmcnt(2)
	v_mul_f32_e32 v43, 0x42800000, v92
	v_mul_f32_e32 v40, 0x42800000, v89
	ds_write2_b32 v8, v4, v43 offset0:96 offset1:104
	v_mul_f32_e32 v4, 0x42800000, v93
	v_mul_f32_e32 v41, 0x42800000, v90
	ds_write2_b32 v8, v40, v4 offset0:225 offset1:233
	v_mul_f32_e32 v4, 0x42800000, v94
	v_mul_f32_e32 v42, 0x42800000, v91
	ds_write2_b32 v38, v41, v4 offset0:98 offset1:106
	v_mul_f32_e32 v4, 0x42800000, v95
	ds_write2_b32 v38, v42, v4 offset0:227 offset1:235
	s_waitcnt vmcnt(1)
	v_mul_f32_e32 v4, 0x42800000, v96
	s_waitcnt vmcnt(0)
	v_mul_f32_e32 v43, 0x42800000, v100
	v_mul_f32_e32 v40, 0x42800000, v97
	ds_write2_b32 v8, v4, v43 offset0:112 offset1:120
	v_mul_f32_e32 v4, 0x42800000, v101
	v_mul_f32_e32 v41, 0x42800000, v98
	ds_write2_b32 v8, v40, v4 offset0:241 offset1:249
	v_mul_f32_e32 v4, 0x42800000, v102
	v_mul_f32_e32 v42, 0x42800000, v99
	ds_write2_b32 v38, v41, v4 offset0:114 offset1:122
	v_mul_f32_e32 v4, 0x42800000, v103
	ds_write2_b32 v38, v42, v4 offset0:243 offset1:251
	s_waitcnt lgkmcnt(0)
	ds_read2_b32 v[40:41], v13 offset1:1
	ds_read2_b32 v[42:43], v13 offset0:2 offset1:3
	ds_read2_b32 v[44:45], v13 offset0:4 offset1:5
	ds_read2_b32 v[46:47], v13 offset0:6 offset1:7
	s_waitcnt lgkmcnt(3)
	v_med3_f32 v4, v40, s33, v39
	v_med3_f32 v41, v41, s33, v39
	v_mov_b32_e32 v40, v5
	v_cvt_pk_fp8_f32 v40, v4, v41
	s_waitcnt lgkmcnt(2)
	v_med3_f32 v4, v42, s33, v39
	v_med3_f32 v41, v43, s33, v39
	s_waitcnt lgkmcnt(1)
	v_med3_f32 v42, v45, s33, v39
	v_cvt_pk_fp8_f32 v40, v4, v41 op_sel:[0,0,1]
	v_med3_f32 v4, v44, s33, v39
	v_mov_b32_e32 v41, v5
	v_cvt_pk_fp8_f32 v41, v4, v42
	ds_read2_b32 v[42:43], v13 offset0:8 offset1:9
	s_waitcnt lgkmcnt(1)
	v_med3_f32 v4, v46, s33, v39
	v_med3_f32 v44, v47, s33, v39
	v_cvt_pk_fp8_f32 v41, v4, v44 op_sel:[0,0,1]
	ds_read2_b32 v[44:45], v13 offset0:10 offset1:11
	ds_read2_b32 v[46:47], v13 offset0:12 offset1:13
	ds_read2_b32 v[50:51], v13 offset0:14 offset1:15
	s_waitcnt lgkmcnt(3)
	v_med3_f32 v4, v42, s33, v39
	v_med3_f32 v43, v43, s33, v39
	v_mov_b32_e32 v42, v5
	v_cvt_pk_fp8_f32 v42, v4, v43
	s_waitcnt lgkmcnt(2)
	v_med3_f32 v4, v44, s33, v39
	v_med3_f32 v44, v45, s33, v39
	s_waitcnt lgkmcnt(1)
	v_med3_f32 v45, v46, s33, v39
	v_med3_f32 v46, v47, s33, v39
	v_mov_b32_e32 v43, v5
	v_cvt_pk_fp8_f32 v43, v45, v46
	v_cvt_pk_fp8_f32 v42, v4, v44 op_sel:[0,0,1]
	s_waitcnt lgkmcnt(0)
	v_med3_f32 v4, v50, s33, v39
	v_med3_f32 v44, v51, s33, v39
	v_cvt_pk_fp8_f32 v43, v4, v44 op_sel:[0,0,1]
	ds_read2_b32 v[44:45], v14 offset1:1
	v_or_b32_e32 v4, s2, v7
	v_lshlrev_b32_e32 v4, 10, v4
	v_lshl_add_u64 v[46:47], v[48:49], 0, v[4:5]
	ds_read2_b32 v[50:51], v15 offset1:1
	ds_read2_b32 v[52:53], v16 offset1:1
	ds_read2_b32 v[54:55], v17 offset1:1
	s_waitcnt lgkmcnt(3)
	v_med3_f32 v4, v44, s33, v39
	v_med3_f32 v45, v45, s33, v39
	v_mov_b32_e32 v44, v5
	v_cvt_pk_fp8_f32 v44, v4, v45
	global_store_dwordx4 v[46:47], v[40:43], off nt
	s_waitcnt lgkmcnt(2)
	v_med3_f32 v4, v50, s33, v39
	v_mov_b32_e32 v45, v5
	v_med3_f32 v40, v51, s33, v39
	v_cvt_pk_fp8_f32 v44, v4, v40 op_sel:[0,0,1]
	s_waitcnt lgkmcnt(1)
	v_med3_f32 v4, v52, s33, v39
	v_med3_f32 v40, v53, s33, v39
	v_cvt_pk_fp8_f32 v45, v4, v40
	ds_read2_b32 v[40:41], v18 offset1:1
	s_waitcnt lgkmcnt(1)
	v_med3_f32 v4, v54, s33, v39
	v_med3_f32 v42, v55, s33, v39
	v_cvt_pk_fp8_f32 v45, v4, v42 op_sel:[0,0,1]
	ds_read2_b32 v[42:43], v19 offset1:1
	ds_read2_b32 v[50:51], v20 offset1:1
	ds_read2_b32 v[52:53], v21 offset1:1
	s_waitcnt lgkmcnt(3)
	v_med3_f32 v4, v40, s33, v39
	v_med3_f32 v40, v41, s33, v39
	v_mov_b32_e32 v46, v5
	v_cvt_pk_fp8_f32 v46, v4, v40
	s_waitcnt lgkmcnt(2)
	v_med3_f32 v4, v42, s33, v39
	s_waitcnt lgkmcnt(1)
	v_med3_f32 v41, v50, s33, v39
	v_med3_f32 v42, v51, s33, v39
	v_mov_b32_e32 v47, v5
	v_cvt_pk_fp8_f32 v47, v41, v42
	v_med3_f32 v40, v43, s33, v39
	v_cvt_pk_fp8_f32 v46, v4, v40 op_sel:[0,0,1]
	s_waitcnt lgkmcnt(0)
	v_med3_f32 v4, v52, s33, v39
	v_med3_f32 v40, v53, s33, v39
	v_cvt_pk_fp8_f32 v47, v4, v40 op_sel:[0,0,1]
	ds_read2_b32 v[40:41], v22 offset1:1
	v_or_b32_e32 v4, s2, v9
	v_lshlrev_b32_e32 v4, 10, v4
	v_lshl_add_u64 v[42:43], v[48:49], 0, v[4:5]
	ds_read2_b32 v[50:51], v23 offset1:1
	ds_read2_b32 v[52:53], v24 offset1:1
	ds_read2_b32 v[54:55], v25 offset1:1
	s_waitcnt lgkmcnt(3)
	v_med3_f32 v4, v40, s33, v39
	v_med3_f32 v41, v41, s33, v39
	v_mov_b32_e32 v40, v5
	v_cvt_pk_fp8_f32 v40, v4, v41
	s_waitcnt lgkmcnt(2)
	v_med3_f32 v4, v50, s33, v39
	v_med3_f32 v41, v51, s33, v39
	global_store_dwordx4 v[42:43], v[44:47], off nt
	v_cvt_pk_fp8_f32 v40, v4, v41 op_sel:[0,0,1]
	s_waitcnt lgkmcnt(1)
	v_med3_f32 v4, v52, s33, v39
	v_med3_f32 v42, v53, s33, v39
	v_mov_b32_e32 v41, v5
	v_cvt_pk_fp8_f32 v41, v4, v42
	ds_read2_b32 v[42:43], v26 offset1:1
	s_waitcnt lgkmcnt(1)
	v_med3_f32 v4, v54, s33, v39
	v_med3_f32 v44, v55, s33, v39
	v_cvt_pk_fp8_f32 v41, v4, v44 op_sel:[0,0,1]
	ds_read2_b32 v[44:45], v27 offset1:1
	ds_read2_b32 v[46:47], v28 offset1:1
	ds_read2_b32 v[50:51], v29 offset1:1
	s_waitcnt lgkmcnt(3)
	v_med3_f32 v4, v42, s33, v39
	v_med3_f32 v43, v43, s33, v39
	v_mov_b32_e32 v42, v5
	v_cvt_pk_fp8_f32 v42, v4, v43
	s_waitcnt lgkmcnt(2)
	v_med3_f32 v4, v44, s33, v39
	v_med3_f32 v44, v45, s33, v39
	s_waitcnt lgkmcnt(1)
	v_med3_f32 v45, v46, s33, v39
	v_med3_f32 v46, v47, s33, v39
	v_mov_b32_e32 v43, v5
	v_cvt_pk_fp8_f32 v43, v45, v46
	v_cvt_pk_fp8_f32 v42, v4, v44 op_sel:[0,0,1]
	s_waitcnt lgkmcnt(0)
	v_med3_f32 v4, v50, s33, v39
	v_med3_f32 v44, v51, s33, v39
	v_cvt_pk_fp8_f32 v43, v4, v44 op_sel:[0,0,1]
	ds_read2_b32 v[44:45], v30 offset1:1
	v_or_b32_e32 v4, s2, v10
	v_lshlrev_b32_e32 v4, 10, v4
	v_lshl_add_u64 v[46:47], v[48:49], 0, v[4:5]
	ds_read2_b32 v[50:51], v31 offset1:1
	ds_read2_b32 v[52:53], v32 offset1:1
	ds_read2_b32 v[54:55], v33 offset1:1
	s_waitcnt lgkmcnt(3)
	v_med3_f32 v4, v44, s33, v39
	v_med3_f32 v45, v45, s33, v39
	v_mov_b32_e32 v44, v5
	v_cvt_pk_fp8_f32 v44, v4, v45
	global_store_dwordx4 v[46:47], v[40:43], off nt
	s_waitcnt lgkmcnt(2)
	v_med3_f32 v4, v50, s33, v39
	v_mov_b32_e32 v45, v5
	v_med3_f32 v40, v51, s33, v39
	v_cvt_pk_fp8_f32 v44, v4, v40 op_sel:[0,0,1]
	s_waitcnt lgkmcnt(1)
	v_med3_f32 v4, v52, s33, v39
	v_med3_f32 v40, v53, s33, v39
	v_cvt_pk_fp8_f32 v45, v4, v40
	ds_read2_b32 v[40:41], v34 offset1:1
	s_waitcnt lgkmcnt(1)
	v_med3_f32 v4, v54, s33, v39
	v_med3_f32 v42, v55, s33, v39
	v_cvt_pk_fp8_f32 v45, v4, v42 op_sel:[0,0,1]
	ds_read2_b32 v[42:43], v35 offset1:1
	ds_read2_b32 v[50:51], v36 offset1:1
	ds_read2_b32 v[52:53], v37 offset1:1
	s_waitcnt lgkmcnt(3)
	v_med3_f32 v4, v40, s33, v39
	v_med3_f32 v40, v41, s33, v39
	v_mov_b32_e32 v46, v5
	v_cvt_pk_fp8_f32 v46, v4, v40
	s_waitcnt lgkmcnt(2)
	v_med3_f32 v4, v42, s33, v39
	s_waitcnt lgkmcnt(1)
	v_med3_f32 v41, v50, s33, v39
	v_med3_f32 v42, v51, s33, v39
	v_mov_b32_e32 v47, v5
	v_cvt_pk_fp8_f32 v47, v41, v42
	v_med3_f32 v40, v43, s33, v39
	v_cvt_pk_fp8_f32 v46, v4, v40 op_sel:[0,0,1]
	s_waitcnt lgkmcnt(0)
	v_med3_f32 v4, v52, s33, v39
	v_med3_f32 v40, v53, s33, v39
	v_cvt_pk_fp8_f32 v47, v4, v40 op_sel:[0,0,1]
	v_or_b32_e32 v4, s2, v11
	v_lshlrev_b32_e32 v4, 10, v4
	v_lshl_add_u64 v[40:41], v[48:49], 0, v[4:5]
	global_store_dwordx4 v[40:41], v[44:47], off nt
	s_waitcnt lgkmcnt(0)
.LBB0_469:
	s_andn2_b64 vcc, exec, s[4:5]
	s_cbranch_vccnz .LBB0_457
	v_readlane_b32 s60, v255, 3
	s_lshr_b32 s2, s6, 9
	v_readlane_b32 s68, v255, 11
	v_readlane_b32 s69, v255, 12
	v_readlane_b32 s70, v255, 13
	v_readlane_b32 s71, v255, 14
	v_readlane_b32 s72, v255, 15
	v_readlane_b32 s73, v255, 16
	s_lshl_b64 s[4:5], s[2:3], 23
	v_readlane_b32 s74, v255, 17
	v_readlane_b32 s75, v255, 18
	s_mov_b64 s[68:69], s[72:73]
	s_add_u32 s44, s68, s4
	s_addc_u32 s45, s69, s5
	s_lshl_b64 s[8:9], s[2:3], 21
	s_add_u32 s5, s12, s8
	s_addc_u32 s4, s13, s9
	s_lshl_b32 s2, s6, 1
	s_and_b32 s8, s2, 0x380
	s_and_b32 s2, s7, 0x7e0
	s_and_b32 s7, s7, 0xe0
	s_cmpk_lt_u32 s7, 0x80
	s_cselect_b64 vcc, -1, 0
	s_lshl_b32 s6, s6, 4
	v_or_b32_e32 v4, s7, v6
	s_and_b32 s6, s6, 0x380
	v_or_b32_e32 v40, s6, v4
	s_addk_i32 s6, 0x380
	v_add_u32_e32 v4, s6, v4
	v_cndmask_b32_e32 v4, v4, v40, vcc
	v_or_b32_e32 v42, s8, v7
	v_lshlrev_b32_e32 v4, 2, v4
	v_lshl_add_u64 v[40:41], s[44:45], 0, v[4:5]
	v_lshlrev_b32_e32 v4, 13, v42
	v_lshl_add_u64 v[96:97], v[40:41], 0, v[4:5]
	v_add_co_u32_e32 v44, vcc, s18, v96
	global_load_dwordx4 v[40:43], v[96:97], off
	s_nop 0
	v_addc_co_u32_e32 v45, vcc, 0, v97, vcc
	global_load_dwordx4 v[44:47], v[44:45], off
	v_add_co_u32_e32 v48, vcc, s20, v96
	s_add_u32 s6, s5, s8
	s_nop 0
	v_addc_co_u32_e32 v49, vcc, 0, v97, vcc
	v_add_co_u32_e32 v52, vcc, s22, v96
	global_load_dwordx4 v[48:51], v[48:49], off
	s_nop 0
	v_addc_co_u32_e32 v53, vcc, 0, v97, vcc
	global_load_dwordx4 v[52:55], v[52:53], off
	v_add_co_u32_e32 v56, vcc, s24, v96
	s_addc_u32 s7, s4, 0
	s_nop 0
	v_addc_co_u32_e32 v57, vcc, 0, v97, vcc
	v_add_co_u32_e32 v60, vcc, s26, v96
	global_load_dwordx4 v[56:59], v[56:57], off
	s_nop 0
	v_addc_co_u32_e32 v61, vcc, 0, v97, vcc
	global_load_dwordx4 v[60:63], v[60:61], off
	v_add_co_u32_e32 v64, vcc, s28, v96
	v_readlane_b32 s61, v255, 4
	s_nop 0
	v_addc_co_u32_e32 v65, vcc, 0, v97, vcc
	v_add_co_u32_e32 v68, vcc, s30, v96
	global_load_dwordx4 v[64:67], v[64:65], off
	s_nop 0
	v_addc_co_u32_e32 v69, vcc, 0, v97, vcc
	global_load_dwordx4 v[68:71], v[68:69], off
	v_add_co_u32_e32 v72, vcc, s34, v96
	v_readlane_b32 s62, v255, 5
	s_nop 0
	v_addc_co_u32_e32 v73, vcc, 0, v97, vcc
	v_add_co_u32_e32 v76, vcc, s35, v96
	v_readlane_b32 s63, v255, 6
	s_nop 0
	v_addc_co_u32_e32 v77, vcc, 0, v97, vcc
	global_load_dwordx4 v[72:75], v[72:73], off
	s_nop 0
	global_load_dwordx4 v[76:79], v[76:77], off
	v_add_co_u32_e32 v80, vcc, s38, v96
	v_readlane_b32 s64, v255, 7
	s_nop 0
	v_addc_co_u32_e32 v81, vcc, 0, v97, vcc
	v_add_co_u32_e32 v84, vcc, s39, v96
	v_readlane_b32 s65, v255, 8
	s_nop 0
	v_addc_co_u32_e32 v85, vcc, 0, v97, vcc
	global_load_dwordx4 v[80:83], v[80:81], off
	s_nop 0
	global_load_dwordx4 v[84:87], v[84:85], off
	v_add_co_u32_e32 v88, vcc, s40, v96
	v_readlane_b32 s66, v255, 9
	s_nop 0
	v_addc_co_u32_e32 v89, vcc, 0, v97, vcc
	v_add_co_u32_e32 v92, vcc, s41, v96
	v_readlane_b32 s67, v255, 10
	s_nop 0
	v_addc_co_u32_e32 v93, vcc, 0, v97, vcc
	global_load_dwordx4 v[88:91], v[88:89], off
	s_nop 0
	global_load_dwordx4 v[92:95], v[92:93], off
	v_add_co_u32_e32 v98, vcc, s42, v96
	s_mov_b64 s[70:71], s[74:75]
	s_nop 0
	v_addc_co_u32_e32 v99, vcc, 0, v97, vcc
	v_add_co_u32_e32 v100, vcc, s43, v96
	s_waitcnt vmcnt(13)
	v_mul_f32_e32 v4, 0x42800000, v40
	v_addc_co_u32_e32 v101, vcc, 0, v97, vcc
	global_load_dwordx4 v[96:99], v[98:99], off
	s_nop 0
	global_load_dwordx4 v[100:103], v[100:101], off
	v_mul_f32_e32 v40, 0x42800000, v41
	v_mul_f32_e32 v41, 0x42800000, v42
	v_mul_f32_e32 v42, 0x42800000, v43
	s_waitcnt vmcnt(14)
	v_mul_f32_e32 v43, 0x42800000, v44
	ds_write2_b32 v8, v4, v43 offset1:8
	v_mul_f32_e32 v4, 0x42800000, v45
	ds_write2_b32 v8, v40, v4 offset0:129 offset1:137
	v_mul_f32_e32 v4, 0x42800000, v46
	ds_write2_b32 v38, v41, v4 offset0:2 offset1:10
	v_mul_f32_e32 v4, 0x42800000, v47
	ds_write2_b32 v38, v42, v4 offset0:131 offset1:139
	s_waitcnt vmcnt(13)
	v_mul_f32_e32 v4, 0x42800000, v48
	s_waitcnt vmcnt(12)
	v_mul_f32_e32 v43, 0x42800000, v52
	v_mul_f32_e32 v40, 0x42800000, v49
	ds_write2_b32 v8, v4, v43 offset0:16 offset1:24
	v_mul_f32_e32 v4, 0x42800000, v53
	v_mul_f32_e32 v41, 0x42800000, v50
	ds_write2_b32 v8, v40, v4 offset0:145 offset1:153
	v_mul_f32_e32 v4, 0x42800000, v54
	v_mul_f32_e32 v42, 0x42800000, v51
	ds_write2_b32 v38, v41, v4 offset0:18 offset1:26
	v_mul_f32_e32 v4, 0x42800000, v55
	ds_write2_b32 v38, v42, v4 offset0:147 offset1:155
	s_waitcnt vmcnt(11)
	v_mul_f32_e32 v4, 0x42800000, v56
	s_waitcnt vmcnt(10)
	v_mul_f32_e32 v43, 0x42800000, v60
	v_mul_f32_e32 v40, 0x42800000, v57
	ds_write2_b32 v8, v4, v43 offset0:32 offset1:40
	v_mul_f32_e32 v4, 0x42800000, v61
	v_mul_f32_e32 v41, 0x42800000, v58
	ds_write2_b32 v8, v40, v4 offset0:161 offset1:169
	v_mul_f32_e32 v4, 0x42800000, v62
	v_mul_f32_e32 v42, 0x42800000, v59
	ds_write2_b32 v38, v41, v4 offset0:34 offset1:42
	v_mul_f32_e32 v4, 0x42800000, v63
	ds_write2_b32 v38, v42, v4 offset0:163 offset1:171
	s_waitcnt vmcnt(9)
	v_mul_f32_e32 v4, 0x42800000, v64
	s_waitcnt vmcnt(8)
	v_mul_f32_e32 v43, 0x42800000, v68
	v_mul_f32_e32 v40, 0x42800000, v65
	ds_write2_b32 v8, v4, v43 offset0:48 offset1:56
	v_mul_f32_e32 v4, 0x42800000, v69
	v_mul_f32_e32 v41, 0x42800000, v66
	ds_write2_b32 v8, v40, v4 offset0:177 offset1:185
	v_mul_f32_e32 v4, 0x42800000, v70
	v_mul_f32_e32 v42, 0x42800000, v67
	ds_write2_b32 v38, v41, v4 offset0:50 offset1:58
	v_mul_f32_e32 v4, 0x42800000, v71
	ds_write2_b32 v38, v42, v4 offset0:179 offset1:187
	s_waitcnt vmcnt(7)
	v_mul_f32_e32 v4, 0x42800000, v72
	s_waitcnt vmcnt(6)
	v_mul_f32_e32 v43, 0x42800000, v76
	v_mul_f32_e32 v40, 0x42800000, v73
	ds_write2_b32 v8, v4, v43 offset0:64 offset1:72
	v_mul_f32_e32 v4, 0x42800000, v77
	v_mul_f32_e32 v41, 0x42800000, v74
	ds_write2_b32 v8, v40, v4 offset0:193 offset1:201
	v_mul_f32_e32 v4, 0x42800000, v78
	v_mul_f32_e32 v42, 0x42800000, v75
	ds_write2_b32 v38, v41, v4 offset0:66 offset1:74
	v_mul_f32_e32 v4, 0x42800000, v79
	ds_write2_b32 v38, v42, v4 offset0:195 offset1:203
	s_waitcnt vmcnt(5)
	v_mul_f32_e32 v4, 0x42800000, v80
	s_waitcnt vmcnt(4)
	v_mul_f32_e32 v43, 0x42800000, v84
	v_mul_f32_e32 v40, 0x42800000, v81
	ds_write2_b32 v8, v4, v43 offset0:80 offset1:88
	v_mul_f32_e32 v4, 0x42800000, v85
	v_mul_f32_e32 v41, 0x42800000, v82
	ds_write2_b32 v8, v40, v4 offset0:209 offset1:217
	v_mul_f32_e32 v4, 0x42800000, v86
	v_mul_f32_e32 v42, 0x42800000, v83
	ds_write2_b32 v38, v41, v4 offset0:82 offset1:90
	v_mul_f32_e32 v4, 0x42800000, v87
	ds_write2_b32 v38, v42, v4 offset0:211 offset1:219
	s_waitcnt vmcnt(3)
	v_mul_f32_e32 v4, 0x42800000, v88
	s_waitcnt vmcnt(2)
	v_mul_f32_e32 v43, 0x42800000, v92
	v_mul_f32_e32 v40, 0x42800000, v89
	ds_write2_b32 v8, v4, v43 offset0:96 offset1:104
	v_mul_f32_e32 v4, 0x42800000, v93
	v_mul_f32_e32 v41, 0x42800000, v90
	ds_write2_b32 v8, v40, v4 offset0:225 offset1:233
	v_mul_f32_e32 v4, 0x42800000, v94
	v_mul_f32_e32 v42, 0x42800000, v91
	ds_write2_b32 v38, v41, v4 offset0:98 offset1:106
	v_mul_f32_e32 v4, 0x42800000, v95
	ds_write2_b32 v38, v42, v4 offset0:227 offset1:235
	s_waitcnt vmcnt(1)
	v_mul_f32_e32 v4, 0x42800000, v96
	s_waitcnt vmcnt(0)
	v_mul_f32_e32 v43, 0x42800000, v100
	v_mul_f32_e32 v40, 0x42800000, v97
	ds_write2_b32 v8, v4, v43 offset0:112 offset1:120
	v_mul_f32_e32 v4, 0x42800000, v101
	v_mul_f32_e32 v41, 0x42800000, v98
	ds_write2_b32 v8, v40, v4 offset0:241 offset1:249
	v_mul_f32_e32 v4, 0x42800000, v102
	v_mul_f32_e32 v42, 0x42800000, v99
	ds_write2_b32 v38, v41, v4 offset0:114 offset1:122
	v_mul_f32_e32 v4, 0x42800000, v103
	ds_write2_b32 v38, v42, v4 offset0:243 offset1:251
	s_waitcnt lgkmcnt(0)
	ds_read2_b32 v[40:41], v13 offset1:1
	ds_read2_b32 v[42:43], v13 offset0:2 offset1:3
	ds_read2_b32 v[44:45], v13 offset0:4 offset1:5
	ds_read2_b32 v[46:47], v13 offset0:6 offset1:7
	v_lshl_add_u64 v[48:49], s[6:7], 0, v[2:3]
	s_waitcnt lgkmcnt(3)
	v_med3_f32 v4, v40, s33, v39
	v_med3_f32 v41, v41, s33, v39
	v_mov_b32_e32 v40, v5
	v_cvt_pk_fp8_f32 v40, v4, v41
	s_waitcnt lgkmcnt(2)
	v_med3_f32 v4, v42, s33, v39
	v_med3_f32 v41, v43, s33, v39
	s_waitcnt lgkmcnt(1)
	v_med3_f32 v42, v45, s33, v39
	v_cvt_pk_fp8_f32 v40, v4, v41 op_sel:[0,0,1]
	v_med3_f32 v4, v44, s33, v39
	v_mov_b32_e32 v41, v5
	v_cvt_pk_fp8_f32 v41, v4, v42
	ds_read2_b32 v[42:43], v13 offset0:8 offset1:9
	s_waitcnt lgkmcnt(1)
	v_med3_f32 v4, v46, s33, v39
	v_med3_f32 v44, v47, s33, v39
	v_cvt_pk_fp8_f32 v41, v4, v44 op_sel:[0,0,1]
	ds_read2_b32 v[44:45], v13 offset0:10 offset1:11
	ds_read2_b32 v[46:47], v13 offset0:12 offset1:13
	ds_read2_b32 v[50:51], v13 offset0:14 offset1:15
	s_waitcnt lgkmcnt(3)
	v_med3_f32 v4, v42, s33, v39
	v_med3_f32 v43, v43, s33, v39
	v_mov_b32_e32 v42, v5
	v_cvt_pk_fp8_f32 v42, v4, v43
	s_waitcnt lgkmcnt(2)
	v_med3_f32 v4, v44, s33, v39
	v_med3_f32 v44, v45, s33, v39
	s_waitcnt lgkmcnt(1)
	v_med3_f32 v45, v46, s33, v39
	v_med3_f32 v46, v47, s33, v39
	v_mov_b32_e32 v43, v5
	v_cvt_pk_fp8_f32 v43, v45, v46
	v_cvt_pk_fp8_f32 v42, v4, v44 op_sel:[0,0,1]
	s_waitcnt lgkmcnt(0)
	v_med3_f32 v4, v50, s33, v39
	v_med3_f32 v44, v51, s33, v39
	v_cvt_pk_fp8_f32 v43, v4, v44 op_sel:[0,0,1]
	ds_read2_b32 v[44:45], v14 offset1:1
	v_or_b32_e32 v4, s2, v7
	v_lshlrev_b32_e32 v4, 10, v4
	v_lshl_add_u64 v[46:47], v[48:49], 0, v[4:5]
	ds_read2_b32 v[50:51], v15 offset1:1
	ds_read2_b32 v[52:53], v16 offset1:1
	ds_read2_b32 v[54:55], v17 offset1:1
	s_waitcnt lgkmcnt(3)
	v_med3_f32 v4, v44, s33, v39
	v_med3_f32 v45, v45, s33, v39
	v_mov_b32_e32 v44, v5
	v_cvt_pk_fp8_f32 v44, v4, v45
	global_store_dwordx4 v[46:47], v[40:43], off nt
	s_waitcnt lgkmcnt(2)
	v_med3_f32 v4, v50, s33, v39
	v_mov_b32_e32 v45, v5
	v_med3_f32 v40, v51, s33, v39
	v_cvt_pk_fp8_f32 v44, v4, v40 op_sel:[0,0,1]
	s_waitcnt lgkmcnt(1)
	v_med3_f32 v4, v52, s33, v39
	v_med3_f32 v40, v53, s33, v39
	v_cvt_pk_fp8_f32 v45, v4, v40
	ds_read2_b32 v[40:41], v18 offset1:1
	s_waitcnt lgkmcnt(1)
	v_med3_f32 v4, v54, s33, v39
	v_med3_f32 v42, v55, s33, v39
	v_cvt_pk_fp8_f32 v45, v4, v42 op_sel:[0,0,1]
	ds_read2_b32 v[42:43], v19 offset1:1
	ds_read2_b32 v[50:51], v20 offset1:1
	ds_read2_b32 v[52:53], v21 offset1:1
	s_waitcnt lgkmcnt(3)
	v_med3_f32 v4, v40, s33, v39
	v_med3_f32 v40, v41, s33, v39
	v_mov_b32_e32 v46, v5
	v_cvt_pk_fp8_f32 v46, v4, v40
	s_waitcnt lgkmcnt(2)
	v_med3_f32 v4, v42, s33, v39
	s_waitcnt lgkmcnt(1)
	v_med3_f32 v41, v50, s33, v39
	v_med3_f32 v42, v51, s33, v39
	v_mov_b32_e32 v47, v5
	v_cvt_pk_fp8_f32 v47, v41, v42
	v_med3_f32 v40, v43, s33, v39
	v_cvt_pk_fp8_f32 v46, v4, v40 op_sel:[0,0,1]
	s_waitcnt lgkmcnt(0)
	v_med3_f32 v4, v52, s33, v39
	v_med3_f32 v40, v53, s33, v39
	v_cvt_pk_fp8_f32 v47, v4, v40 op_sel:[0,0,1]
	ds_read2_b32 v[40:41], v22 offset1:1
	v_or_b32_e32 v4, s2, v9
	v_lshlrev_b32_e32 v4, 10, v4
	v_lshl_add_u64 v[42:43], v[48:49], 0, v[4:5]
	ds_read2_b32 v[50:51], v23 offset1:1
	ds_read2_b32 v[52:53], v24 offset1:1
	ds_read2_b32 v[54:55], v25 offset1:1
	s_waitcnt lgkmcnt(3)
	v_med3_f32 v4, v40, s33, v39
	v_med3_f32 v41, v41, s33, v39
	v_mov_b32_e32 v40, v5
	v_cvt_pk_fp8_f32 v40, v4, v41
	s_waitcnt lgkmcnt(2)
	v_med3_f32 v4, v50, s33, v39
	v_med3_f32 v41, v51, s33, v39
	global_store_dwordx4 v[42:43], v[44:47], off nt
	v_cvt_pk_fp8_f32 v40, v4, v41 op_sel:[0,0,1]
	s_waitcnt lgkmcnt(1)
	v_med3_f32 v4, v52, s33, v39
	v_med3_f32 v42, v53, s33, v39
	v_mov_b32_e32 v41, v5
	v_cvt_pk_fp8_f32 v41, v4, v42
	ds_read2_b32 v[42:43], v26 offset1:1
	s_waitcnt lgkmcnt(1)
	v_med3_f32 v4, v54, s33, v39
	v_med3_f32 v44, v55, s33, v39
	v_cvt_pk_fp8_f32 v41, v4, v44 op_sel:[0,0,1]
	ds_read2_b32 v[44:45], v27 offset1:1
	ds_read2_b32 v[46:47], v28 offset1:1
	ds_read2_b32 v[50:51], v29 offset1:1
	s_waitcnt lgkmcnt(3)
	v_med3_f32 v4, v42, s33, v39
	v_med3_f32 v43, v43, s33, v39
	v_mov_b32_e32 v42, v5
	v_cvt_pk_fp8_f32 v42, v4, v43
	s_waitcnt lgkmcnt(2)
	v_med3_f32 v4, v44, s33, v39
	v_med3_f32 v44, v45, s33, v39
	s_waitcnt lgkmcnt(1)
	v_med3_f32 v45, v46, s33, v39
	v_med3_f32 v46, v47, s33, v39
	v_mov_b32_e32 v43, v5
	v_cvt_pk_fp8_f32 v43, v45, v46
	v_cvt_pk_fp8_f32 v42, v4, v44 op_sel:[0,0,1]
	s_waitcnt lgkmcnt(0)
	v_med3_f32 v4, v50, s33, v39
	v_med3_f32 v44, v51, s33, v39
	v_cvt_pk_fp8_f32 v43, v4, v44 op_sel:[0,0,1]
	ds_read2_b32 v[44:45], v30 offset1:1
	v_or_b32_e32 v4, s2, v10
	v_lshlrev_b32_e32 v4, 10, v4
	v_lshl_add_u64 v[46:47], v[48:49], 0, v[4:5]
	ds_read2_b32 v[50:51], v31 offset1:1
	ds_read2_b32 v[52:53], v32 offset1:1
	ds_read2_b32 v[54:55], v33 offset1:1
	s_waitcnt lgkmcnt(3)
	v_med3_f32 v4, v44, s33, v39
	v_med3_f32 v45, v45, s33, v39
	v_mov_b32_e32 v44, v5
	v_cvt_pk_fp8_f32 v44, v4, v45
	global_store_dwordx4 v[46:47], v[40:43], off nt
	s_waitcnt lgkmcnt(2)
	v_med3_f32 v4, v50, s33, v39
	v_mov_b32_e32 v45, v5
	v_med3_f32 v40, v51, s33, v39
	v_cvt_pk_fp8_f32 v44, v4, v40 op_sel:[0,0,1]
	s_waitcnt lgkmcnt(1)
	v_med3_f32 v4, v52, s33, v39
	v_med3_f32 v40, v53, s33, v39
	v_cvt_pk_fp8_f32 v45, v4, v40
	ds_read2_b32 v[40:41], v34 offset1:1
	s_waitcnt lgkmcnt(1)
	v_med3_f32 v4, v54, s33, v39
	v_med3_f32 v42, v55, s33, v39
	v_cvt_pk_fp8_f32 v45, v4, v42 op_sel:[0,0,1]
	ds_read2_b32 v[42:43], v35 offset1:1
	ds_read2_b32 v[50:51], v36 offset1:1
	ds_read2_b32 v[52:53], v37 offset1:1
	s_waitcnt lgkmcnt(3)
	v_med3_f32 v4, v40, s33, v39
	v_med3_f32 v40, v41, s33, v39
	v_mov_b32_e32 v46, v5
	v_cvt_pk_fp8_f32 v46, v4, v40
	s_waitcnt lgkmcnt(2)
	v_med3_f32 v4, v42, s33, v39
	s_waitcnt lgkmcnt(1)
	v_med3_f32 v41, v50, s33, v39
	v_med3_f32 v42, v51, s33, v39
	v_mov_b32_e32 v47, v5
	v_cvt_pk_fp8_f32 v47, v41, v42
	v_med3_f32 v40, v43, s33, v39
	v_cvt_pk_fp8_f32 v46, v4, v40 op_sel:[0,0,1]
	s_waitcnt lgkmcnt(0)
	v_med3_f32 v4, v52, s33, v39
	v_med3_f32 v40, v53, s33, v39
	v_cvt_pk_fp8_f32 v47, v4, v40 op_sel:[0,0,1]
	v_or_b32_e32 v4, s2, v11
	v_lshlrev_b32_e32 v4, 10, v4
	v_lshl_add_u64 v[40:41], v[48:49], 0, v[4:5]
	global_store_dwordx4 v[40:41], v[44:47], off nt
	s_waitcnt lgkmcnt(0)
	s_branch .LBB0_457

.LBB0_627:
	s_or_b64 exec, exec, s[4:5]
	s_waitcnt lgkmcnt(0)
	s_barrier
	ds_read_b32 v4, v12
	s_mov_b64 s[4:5], -1
	s_waitcnt lgkmcnt(0)
	v_cmp_lt_u32_e32 vcc, s17, v4
	v_readfirstlane_b32 s2, v4
	s_cbranch_vccnz .LBB0_620
	s_lshl_b32 s6, s2, 3
	s_add_i32 s6, s6, s91
	s_cmpk_gt_u32 s6, 0x5fff
	s_cbranch_scc1 .LBB0_619
	s_lshl_b32 s7, s6, 5
	s_cmpk_gt_u32 s6, 0x3fff
	s_cbranch_scc0 .LBB0_631
	s_add_i32 s2, s6, 0xffffc000
	s_lshr_b32 s2, s2, 8
	s_lshl_b64 s[4:5], s[2:3], 20
	s_lshl_b64 s[8:9], s[2:3], 22
	s_add_u32 s8, s76, s8
	s_addc_u32 s9, s77, s9
	s_add_u32 s4, s10, s4
	s_addc_u32 s5, s11, s5
	s_lshl_b32 s2, s6, 2
	s_and_b32 s45, s2, 0x380
	s_and_b32 s2, s7, 0x3e0
	v_or_b32_e32 v4, s2, v7
	v_or_b32_e32 v42, s45, v1
	v_lshlrev_b32_e32 v4, 2, v4
	v_lshl_add_u64 v[40:41], s[8:9], 0, v[4:5]
	v_lshlrev_b32_e32 v4, 12, v42
	v_lshl_add_u64 v[96:97], v[40:41], 0, v[4:5]
	v_add_co_u32_e32 v44, vcc, s18, v96
	global_load_dwordx4 v[40:43], v[96:97], off
	s_nop 0
	v_addc_co_u32_e32 v45, vcc, 0, v97, vcc
	global_load_dwordx4 v[44:47], v[44:45], off
	v_add_co_u32_e32 v48, vcc, s19, v96
	s_add_u32 s4, s4, s45
	s_nop 0
	v_addc_co_u32_e32 v49, vcc, 0, v97, vcc
	v_add_co_u32_e32 v52, vcc, s20, v96
	global_load_dwordx4 v[48:51], v[48:49], off
	s_nop 0
	v_addc_co_u32_e32 v53, vcc, 0, v97, vcc
	global_load_dwordx4 v[52:55], v[52:53], off
	v_add_co_u32_e32 v56, vcc, s21, v96
	s_addc_u32 s5, s5, 0
	s_nop 0
	v_addc_co_u32_e32 v57, vcc, 0, v97, vcc
	v_add_co_u32_e32 v60, vcc, s22, v96
	global_load_dwordx4 v[56:59], v[56:57], off
	s_nop 0
	v_addc_co_u32_e32 v61, vcc, 0, v97, vcc
	global_load_dwordx4 v[60:63], v[60:61], off
	v_add_co_u32_e32 v64, vcc, s23, v96
	s_nop 1
	v_addc_co_u32_e32 v65, vcc, 0, v97, vcc
	v_add_co_u32_e32 v68, vcc, s24, v96
	global_load_dwordx4 v[64:67], v[64:65], off
	s_nop 0
	v_addc_co_u32_e32 v69, vcc, 0, v97, vcc
	global_load_dwordx4 v[68:71], v[68:69], off
	v_add_co_u32_e32 v72, vcc, s25, v96
	s_waitcnt vmcnt(7)
	v_mul_f32_e32 v4, 0x42800000, v40
	v_addc_co_u32_e32 v73, vcc, 0, v97, vcc
	v_add_co_u32_e32 v76, vcc, s26, v96
	v_mul_f32_e32 v40, 0x42800000, v41
	s_nop 0
	v_addc_co_u32_e32 v77, vcc, 0, v97, vcc
	global_load_dwordx4 v[72:75], v[72:73], off
	s_nop 0
	global_load_dwordx4 v[76:79], v[76:77], off
	v_add_co_u32_e32 v80, vcc, s27, v96
	v_mul_f32_e32 v41, 0x42800000, v42
	s_nop 0
	v_addc_co_u32_e32 v81, vcc, 0, v97, vcc
	v_add_co_u32_e32 v84, vcc, s28, v96
	v_mul_f32_e32 v42, 0x42800000, v43
	s_nop 0
	v_addc_co_u32_e32 v85, vcc, 0, v97, vcc
	global_load_dwordx4 v[80:83], v[80:81], off
	s_nop 0
	global_load_dwordx4 v[84:87], v[84:85], off
	v_add_co_u32_e32 v88, vcc, s29, v96
	s_waitcnt vmcnt(10)
	v_mul_f32_e32 v43, 0x42800000, v44
	v_addc_co_u32_e32 v89, vcc, 0, v97, vcc
	v_add_co_u32_e32 v92, vcc, s30, v96
	s_nop 1
	v_addc_co_u32_e32 v93, vcc, 0, v97, vcc
	global_load_dwordx4 v[88:91], v[88:89], off
	s_nop 0
	global_load_dwordx4 v[92:95], v[92:93], off
	v_add_co_u32_e32 v98, vcc, s31, v96
	s_nop 1
	v_addc_co_u32_e32 v99, vcc, 0, v97, vcc
	v_add_co_u32_e32 v100, vcc, s33, v96
	s_nop 1
	v_addc_co_u32_e32 v101, vcc, 0, v97, vcc
	global_load_dwordx4 v[96:99], v[98:99], off
	s_nop 0
	global_load_dwordx4 v[100:103], v[100:101], off
	ds_write2_b32 v8, v4, v43 offset1:8
	v_mul_f32_e32 v4, 0x42800000, v45
	ds_write2_b32 v8, v40, v4 offset0:129 offset1:137
	v_mul_f32_e32 v4, 0x42800000, v46
	ds_write2_b32 v38, v41, v4 offset0:2 offset1:10
	v_mul_f32_e32 v4, 0x42800000, v47
	ds_write2_b32 v38, v42, v4 offset0:131 offset1:139
	s_waitcnt vmcnt(13)
	v_mul_f32_e32 v4, 0x42800000, v48
	s_waitcnt vmcnt(12)
	v_mul_f32_e32 v43, 0x42800000, v52
	v_mul_f32_e32 v40, 0x42800000, v49
	ds_write2_b32 v8, v4, v43 offset0:16 offset1:24
	v_mul_f32_e32 v4, 0x42800000, v53
	v_mul_f32_e32 v41, 0x42800000, v50
	ds_write2_b32 v8, v40, v4 offset0:145 offset1:153
	v_mul_f32_e32 v4, 0x42800000, v54
	v_mul_f32_e32 v42, 0x42800000, v51
	ds_write2_b32 v38, v41, v4 offset0:18 offset1:26
	v_mul_f32_e32 v4, 0x42800000, v55
	ds_write2_b32 v38, v42, v4 offset0:147 offset1:155
	s_waitcnt vmcnt(11)
	v_mul_f32_e32 v4, 0x42800000, v56
	s_waitcnt vmcnt(10)
	v_mul_f32_e32 v43, 0x42800000, v60
	v_mul_f32_e32 v40, 0x42800000, v57
	ds_write2_b32 v8, v4, v43 offset0:32 offset1:40
	v_mul_f32_e32 v4, 0x42800000, v61
	v_mul_f32_e32 v41, 0x42800000, v58
	ds_write2_b32 v8, v40, v4 offset0:161 offset1:169
	v_mul_f32_e32 v4, 0x42800000, v62
	v_mul_f32_e32 v42, 0x42800000, v59
	ds_write2_b32 v38, v41, v4 offset0:34 offset1:42
	v_mul_f32_e32 v4, 0x42800000, v63
	ds_write2_b32 v38, v42, v4 offset0:163 offset1:171
	s_waitcnt vmcnt(9)
	v_mul_f32_e32 v4, 0x42800000, v64
	s_waitcnt vmcnt(8)
	v_mul_f32_e32 v43, 0x42800000, v68
	v_mul_f32_e32 v40, 0x42800000, v65
	ds_write2_b32 v8, v4, v43 offset0:48 offset1:56
	v_mul_f32_e32 v4, 0x42800000, v69
	v_mul_f32_e32 v41, 0x42800000, v66
	ds_write2_b32 v8, v40, v4 offset0:177 offset1:185
	v_mul_f32_e32 v4, 0x42800000, v70
	v_mul_f32_e32 v42, 0x42800000, v67
	ds_write2_b32 v38, v41, v4 offset0:50 offset1:58
	v_mul_f32_e32 v4, 0x42800000, v71
	ds_write2_b32 v38, v42, v4 offset0:179 offset1:187
	v_lshl_add_u64 v[48:49], s[4:5], 0, v[2:3]
	s_mov_b64 s[4:5], 0
	s_waitcnt vmcnt(7)
	v_mul_f32_e32 v4, 0x42800000, v72
	s_waitcnt vmcnt(6)
	v_mul_f32_e32 v43, 0x42800000, v76
	v_mul_f32_e32 v40, 0x42800000, v73
	ds_write2_b32 v8, v4, v43 offset0:64 offset1:72
	v_mul_f32_e32 v4, 0x42800000, v77
	v_mul_f32_e32 v41, 0x42800000, v74
	ds_write2_b32 v8, v40, v4 offset0:193 offset1:201
	v_mul_f32_e32 v4, 0x42800000, v78
	v_mul_f32_e32 v42, 0x42800000, v75
	ds_write2_b32 v38, v41, v4 offset0:66 offset1:74
	v_mul_f32_e32 v4, 0x42800000, v79
	ds_write2_b32 v38, v42, v4 offset0:195 offset1:203
	s_waitcnt vmcnt(5)
	v_mul_f32_e32 v4, 0x42800000, v80
	s_waitcnt vmcnt(4)
	v_mul_f32_e32 v43, 0x42800000, v84
	v_mul_f32_e32 v40, 0x42800000, v81
	ds_write2_b32 v8, v4, v43 offset0:80 offset1:88
	v_mul_f32_e32 v4, 0x42800000, v85
	v_mul_f32_e32 v41, 0x42800000, v82
	ds_write2_b32 v8, v40, v4 offset0:209 offset1:217
	v_mul_f32_e32 v4, 0x42800000, v86
	v_mul_f32_e32 v42, 0x42800000, v83
	ds_write2_b32 v38, v41, v4 offset0:82 offset1:90
	v_mul_f32_e32 v4, 0x42800000, v87
	ds_write2_b32 v38, v42, v4 offset0:211 offset1:219
	s_waitcnt vmcnt(3)
	v_mul_f32_e32 v4, 0x42800000, v88
	s_waitcnt vmcnt(2)
	v_mul_f32_e32 v43, 0x42800000, v92
	v_mul_f32_e32 v40, 0x42800000, v89
	ds_write2_b32 v8, v4, v43 offset0:96 offset1:104
	v_mul_f32_e32 v4, 0x42800000, v93
	v_mul_f32_e32 v41, 0x42800000, v90
	ds_write2_b32 v8, v40, v4 offset0:225 offset1:233
	v_mul_f32_e32 v4, 0x42800000, v94
	v_mul_f32_e32 v42, 0x42800000, v91
	ds_write2_b32 v38, v41, v4 offset0:98 offset1:106
	v_mul_f32_e32 v4, 0x42800000, v95
	ds_write2_b32 v38, v42, v4 offset0:227 offset1:235
	s_waitcnt vmcnt(1)
	v_mul_f32_e32 v4, 0x42800000, v96
	s_waitcnt vmcnt(0)
	v_mul_f32_e32 v43, 0x42800000, v100
	v_mul_f32_e32 v40, 0x42800000, v97
	ds_write2_b32 v8, v4, v43 offset0:112 offset1:120
	v_mul_f32_e32 v4, 0x42800000, v101
	v_mul_f32_e32 v41, 0x42800000, v98
	ds_write2_b32 v8, v40, v4 offset0:241 offset1:249
	v_mul_f32_e32 v4, 0x42800000, v102
	v_mul_f32_e32 v42, 0x42800000, v99
	ds_write2_b32 v38, v41, v4 offset0:114 offset1:122
	v_mul_f32_e32 v4, 0x42800000, v103
	ds_write2_b32 v38, v42, v4 offset0:243 offset1:251
	s_waitcnt lgkmcnt(0)
	ds_read2_b32 v[40:41], v13 offset1:1
	ds_read2_b32 v[42:43], v13 offset0:2 offset1:3
	ds_read2_b32 v[44:45], v13 offset0:4 offset1:5
	ds_read2_b32 v[46:47], v13 offset0:6 offset1:7
	s_waitcnt lgkmcnt(3)
	v_med3_f32 v4, v40, s34, v39
	v_med3_f32 v41, v41, s34, v39
	v_mov_b32_e32 v40, v5
	v_cvt_pk_fp8_f32 v40, v4, v41
	s_waitcnt lgkmcnt(2)
	v_med3_f32 v4, v42, s34, v39
	v_med3_f32 v41, v43, s34, v39
	s_waitcnt lgkmcnt(1)
	v_med3_f32 v42, v45, s34, v39
	v_cvt_pk_fp8_f32 v40, v4, v41 op_sel:[0,0,1]
	v_med3_f32 v4, v44, s34, v39
	v_mov_b32_e32 v41, v5
	v_cvt_pk_fp8_f32 v41, v4, v42
	ds_read2_b32 v[42:43], v13 offset0:8 offset1:9
	s_waitcnt lgkmcnt(1)
	v_med3_f32 v4, v46, s34, v39
	v_med3_f32 v44, v47, s34, v39
	v_cvt_pk_fp8_f32 v41, v4, v44 op_sel:[0,0,1]
	ds_read2_b32 v[44:45], v13 offset0:10 offset1:11
	ds_read2_b32 v[46:47], v13 offset0:12 offset1:13
	ds_read2_b32 v[50:51], v13 offset0:14 offset1:15
	s_waitcnt lgkmcnt(3)
	v_med3_f32 v4, v42, s34, v39
	v_med3_f32 v43, v43, s34, v39
	v_mov_b32_e32 v42, v5
	v_cvt_pk_fp8_f32 v42, v4, v43
	s_waitcnt lgkmcnt(2)
	v_med3_f32 v4, v44, s34, v39
	v_med3_f32 v44, v45, s34, v39
	s_waitcnt lgkmcnt(1)
	v_med3_f32 v45, v46, s34, v39
	v_med3_f32 v46, v47, s34, v39
	v_mov_b32_e32 v43, v5
	v_cvt_pk_fp8_f32 v43, v45, v46
	v_cvt_pk_fp8_f32 v42, v4, v44 op_sel:[0,0,1]
	s_waitcnt lgkmcnt(0)
	v_med3_f32 v4, v50, s34, v39
	v_med3_f32 v44, v51, s34, v39
	v_cvt_pk_fp8_f32 v43, v4, v44 op_sel:[0,0,1]
	ds_read2_b32 v[44:45], v14 offset1:1
	v_or_b32_e32 v4, s2, v1
	v_lshlrev_b32_e32 v4, 10, v4
	v_lshl_add_u64 v[46:47], v[48:49], 0, v[4:5]
	ds_read2_b32 v[50:51], v15 offset1:1
	ds_read2_b32 v[52:53], v16 offset1:1
	ds_read2_b32 v[54:55], v17 offset1:1
	s_waitcnt lgkmcnt(3)
	v_med3_f32 v4, v44, s34, v39
	v_med3_f32 v45, v45, s34, v39
	v_mov_b32_e32 v44, v5
	v_cvt_pk_fp8_f32 v44, v4, v45
	global_store_dwordx4 v[46:47], v[40:43], off nt
	s_waitcnt lgkmcnt(2)
	v_med3_f32 v4, v50, s34, v39
	v_mov_b32_e32 v45, v5
	v_med3_f32 v40, v51, s34, v39
	v_cvt_pk_fp8_f32 v44, v4, v40 op_sel:[0,0,1]
	s_waitcnt lgkmcnt(1)
	v_med3_f32 v4, v52, s34, v39
	v_med3_f32 v40, v53, s34, v39
	v_cvt_pk_fp8_f32 v45, v4, v40
	ds_read2_b32 v[40:41], v18 offset1:1
	s_waitcnt lgkmcnt(1)
	v_med3_f32 v4, v54, s34, v39
	v_med3_f32 v42, v55, s34, v39
	v_cvt_pk_fp8_f32 v45, v4, v42 op_sel:[0,0,1]
	ds_read2_b32 v[42:43], v19 offset1:1
	ds_read2_b32 v[50:51], v20 offset1:1
	ds_read2_b32 v[52:53], v21 offset1:1
	s_waitcnt lgkmcnt(3)
	v_med3_f32 v4, v40, s34, v39
	v_med3_f32 v40, v41, s34, v39
	v_mov_b32_e32 v46, v5
	v_cvt_pk_fp8_f32 v46, v4, v40
	s_waitcnt lgkmcnt(2)
	v_med3_f32 v4, v42, s34, v39
	s_waitcnt lgkmcnt(1)
	v_med3_f32 v41, v50, s34, v39
	v_med3_f32 v42, v51, s34, v39
	v_mov_b32_e32 v47, v5
	v_cvt_pk_fp8_f32 v47, v41, v42
	v_med3_f32 v40, v43, s34, v39
	v_cvt_pk_fp8_f32 v46, v4, v40 op_sel:[0,0,1]
	s_waitcnt lgkmcnt(0)
	v_med3_f32 v4, v52, s34, v39
	v_med3_f32 v40, v53, s34, v39
	v_cvt_pk_fp8_f32 v47, v4, v40 op_sel:[0,0,1]
	ds_read2_b32 v[40:41], v22 offset1:1
	v_or_b32_e32 v4, s2, v9
	v_lshlrev_b32_e32 v4, 10, v4
	v_lshl_add_u64 v[42:43], v[48:49], 0, v[4:5]
	ds_read2_b32 v[50:51], v23 offset1:1
	ds_read2_b32 v[52:53], v24 offset1:1
	ds_read2_b32 v[54:55], v25 offset1:1
	s_waitcnt lgkmcnt(3)
	v_med3_f32 v4, v40, s34, v39
	v_med3_f32 v41, v41, s34, v39
	v_mov_b32_e32 v40, v5
	v_cvt_pk_fp8_f32 v40, v4, v41
	s_waitcnt lgkmcnt(2)
	v_med3_f32 v4, v50, s34, v39
	v_med3_f32 v41, v51, s34, v39
	global_store_dwordx4 v[42:43], v[44:47], off nt
	v_cvt_pk_fp8_f32 v40, v4, v41 op_sel:[0,0,1]
	s_waitcnt lgkmcnt(1)
	v_med3_f32 v4, v52, s34, v39
	v_med3_f32 v42, v53, s34, v39
	v_mov_b32_e32 v41, v5
	v_cvt_pk_fp8_f32 v41, v4, v42
	ds_read2_b32 v[42:43], v26 offset1:1
	s_waitcnt lgkmcnt(1)
	v_med3_f32 v4, v54, s34, v39
	v_med3_f32 v44, v55, s34, v39
	v_cvt_pk_fp8_f32 v41, v4, v44 op_sel:[0,0,1]
	ds_read2_b32 v[44:45], v27 offset1:1
	ds_read2_b32 v[46:47], v28 offset1:1
	ds_read2_b32 v[50:51], v29 offset1:1
	s_waitcnt lgkmcnt(3)
	v_med3_f32 v4, v42, s34, v39
	v_med3_f32 v43, v43, s34, v39
	v_mov_b32_e32 v42, v5
	v_cvt_pk_fp8_f32 v42, v4, v43
	s_waitcnt lgkmcnt(2)
	v_med3_f32 v4, v44, s34, v39
	v_med3_f32 v44, v45, s34, v39
	s_waitcnt lgkmcnt(1)
	v_med3_f32 v45, v46, s34, v39
	v_med3_f32 v46, v47, s34, v39
	v_mov_b32_e32 v43, v5
	v_cvt_pk_fp8_f32 v43, v45, v46
	v_cvt_pk_fp8_f32 v42, v4, v44 op_sel:[0,0,1]
	s_waitcnt lgkmcnt(0)
	v_med3_f32 v4, v50, s34, v39
	v_med3_f32 v44, v51, s34, v39
	v_cvt_pk_fp8_f32 v43, v4, v44 op_sel:[0,0,1]
	ds_read2_b32 v[44:45], v30 offset1:1
	v_or_b32_e32 v4, s2, v10
	v_lshlrev_b32_e32 v4, 10, v4
	v_lshl_add_u64 v[46:47], v[48:49], 0, v[4:5]
	ds_read2_b32 v[50:51], v31 offset1:1
	ds_read2_b32 v[52:53], v32 offset1:1
	ds_read2_b32 v[54:55], v33 offset1:1
	s_waitcnt lgkmcnt(3)
	v_med3_f32 v4, v44, s34, v39
	v_med3_f32 v45, v45, s34, v39
	v_mov_b32_e32 v44, v5
	v_cvt_pk_fp8_f32 v44, v4, v45
	global_store_dwordx4 v[46:47], v[40:43], off nt
	s_waitcnt lgkmcnt(2)
	v_med3_f32 v4, v50, s34, v39
	v_mov_b32_e32 v45, v5
	v_med3_f32 v40, v51, s34, v39
	v_cvt_pk_fp8_f32 v44, v4, v40 op_sel:[0,0,1]
	s_waitcnt lgkmcnt(1)
	v_med3_f32 v4, v52, s34, v39
	v_med3_f32 v40, v53, s34, v39
	v_cvt_pk_fp8_f32 v45, v4, v40
	ds_read2_b32 v[40:41], v34 offset1:1
	s_waitcnt lgkmcnt(1)
	v_med3_f32 v4, v54, s34, v39
	v_med3_f32 v42, v55, s34, v39
	v_cvt_pk_fp8_f32 v45, v4, v42 op_sel:[0,0,1]
	ds_read2_b32 v[42:43], v35 offset1:1
	ds_read2_b32 v[50:51], v36 offset1:1
	ds_read2_b32 v[52:53], v37 offset1:1
	s_waitcnt lgkmcnt(3)
	v_med3_f32 v4, v40, s34, v39
	v_med3_f32 v40, v41, s34, v39
	v_mov_b32_e32 v46, v5
	v_cvt_pk_fp8_f32 v46, v4, v40
	s_waitcnt lgkmcnt(2)
	v_med3_f32 v4, v42, s34, v39
	s_waitcnt lgkmcnt(1)
	v_med3_f32 v41, v50, s34, v39
	v_med3_f32 v42, v51, s34, v39
	v_mov_b32_e32 v47, v5
	v_cvt_pk_fp8_f32 v47, v41, v42
	v_med3_f32 v40, v43, s34, v39
	v_cvt_pk_fp8_f32 v46, v4, v40 op_sel:[0,0,1]
	s_waitcnt lgkmcnt(0)
	v_med3_f32 v4, v52, s34, v39
	v_med3_f32 v40, v53, s34, v39
	v_cvt_pk_fp8_f32 v47, v4, v40 op_sel:[0,0,1]
	v_or_b32_e32 v4, s2, v11
	v_lshlrev_b32_e32 v4, 10, v4
	v_lshl_add_u64 v[40:41], v[48:49], 0, v[4:5]
	global_store_dwordx4 v[40:41], v[44:47], off nt
	s_waitcnt lgkmcnt(0)
.LBB0_631:
	s_andn2_b64 vcc, exec, s[4:5]
	s_cbranch_vccnz .LBB0_619
	v_readlane_b32 s60, v255, 3
	s_lshr_b32 s2, s6, 9
	v_readlane_b32 s72, v255, 15
	v_readlane_b32 s73, v255, 16
	s_lshl_b64 s[4:5], s[2:3], 23
	v_readlane_b32 s74, v255, 17
	v_readlane_b32 s75, v255, 18
	s_mov_b64 s[52:53], s[72:73]
	s_add_u32 s46, s52, s4
	s_addc_u32 s47, s53, s5
	s_lshl_b64 s[8:9], s[2:3], 21
	s_add_u32 s5, s12, s8
	s_addc_u32 s4, s13, s9
	s_lshl_b32 s2, s6, 1
	s_and_b32 s8, s2, 0x380
	s_and_b32 s2, s7, 0x7e0
	s_and_b32 s7, s7, 0xe0
	s_cmpk_lt_u32 s7, 0x80
	s_cselect_b64 vcc, -1, 0
	s_lshl_b32 s6, s6, 4
	v_or_b32_e32 v4, s7, v7
	s_and_b32 s6, s6, 0x380
	v_or_b32_e32 v40, s6, v4
	s_addk_i32 s6, 0x380
	v_add_u32_e32 v4, s6, v4
	v_cndmask_b32_e32 v4, v4, v40, vcc
	v_or_b32_e32 v42, s8, v1
	v_lshlrev_b32_e32 v4, 2, v4
	v_lshl_add_u64 v[40:41], s[46:47], 0, v[4:5]
	v_lshlrev_b32_e32 v4, 13, v42
	v_lshl_add_u64 v[96:97], v[40:41], 0, v[4:5]
	v_add_co_u32_e32 v44, vcc, s19, v96
	global_load_dwordx4 v[40:43], v[96:97], off
	s_nop 0
	v_addc_co_u32_e32 v45, vcc, 0, v97, vcc
	global_load_dwordx4 v[44:47], v[44:45], off
	v_add_co_u32_e32 v48, vcc, s21, v96
	s_add_u32 s6, s5, s8
	s_nop 0
	v_addc_co_u32_e32 v49, vcc, 0, v97, vcc
	v_add_co_u32_e32 v52, vcc, s23, v96
	global_load_dwordx4 v[48:51], v[48:49], off
	s_nop 0
	v_addc_co_u32_e32 v53, vcc, 0, v97, vcc
	global_load_dwordx4 v[52:55], v[52:53], off
	v_add_co_u32_e32 v56, vcc, s25, v96
	s_addc_u32 s7, s4, 0
	s_nop 0
	v_addc_co_u32_e32 v57, vcc, 0, v97, vcc
	v_add_co_u32_e32 v60, vcc, s27, v96
	global_load_dwordx4 v[56:59], v[56:57], off
	s_nop 0
	v_addc_co_u32_e32 v61, vcc, 0, v97, vcc
	global_load_dwordx4 v[60:63], v[60:61], off
	v_add_co_u32_e32 v64, vcc, s29, v96
	v_readlane_b32 s61, v255, 4
	s_nop 0
	v_addc_co_u32_e32 v65, vcc, 0, v97, vcc
	v_add_co_u32_e32 v68, vcc, s31, v96
	global_load_dwordx4 v[64:67], v[64:65], off
	s_nop 0
	v_addc_co_u32_e32 v69, vcc, 0, v97, vcc
	global_load_dwordx4 v[68:71], v[68:69], off
	v_add_co_u32_e32 v72, vcc, s35, v96
	v_readlane_b32 s62, v255, 5
	s_nop 0
	v_addc_co_u32_e32 v73, vcc, 0, v97, vcc
	v_add_co_u32_e32 v76, vcc, s38, v96
	v_readlane_b32 s63, v255, 6
	s_nop 0
	v_addc_co_u32_e32 v77, vcc, 0, v97, vcc
	global_load_dwordx4 v[72:75], v[72:73], off
	s_nop 0
	global_load_dwordx4 v[76:79], v[76:77], off
	v_add_co_u32_e32 v80, vcc, s39, v96
	v_readlane_b32 s64, v255, 7
	s_nop 0
	v_addc_co_u32_e32 v81, vcc, 0, v97, vcc
	v_add_co_u32_e32 v84, vcc, s40, v96
	v_readlane_b32 s65, v255, 8
	s_nop 0
	v_addc_co_u32_e32 v85, vcc, 0, v97, vcc
	global_load_dwordx4 v[80:83], v[80:81], off
	s_nop 0
	global_load_dwordx4 v[84:87], v[84:85], off
	v_add_co_u32_e32 v88, vcc, s41, v96
	v_readlane_b32 s66, v255, 9
	s_nop 0
	v_addc_co_u32_e32 v89, vcc, 0, v97, vcc
	v_add_co_u32_e32 v92, vcc, s42, v96
	v_readlane_b32 s67, v255, 10
	s_nop 0
	v_addc_co_u32_e32 v93, vcc, 0, v97, vcc
	global_load_dwordx4 v[88:91], v[88:89], off
	s_nop 0
	global_load_dwordx4 v[92:95], v[92:93], off
	v_add_co_u32_e32 v98, vcc, s43, v96
	v_readlane_b32 s68, v255, 11
	s_nop 0
	v_addc_co_u32_e32 v99, vcc, 0, v97, vcc
	v_add_co_u32_e32 v100, vcc, s44, v96
	v_readlane_b32 s69, v255, 12
	s_nop 0
	v_addc_co_u32_e32 v101, vcc, 0, v97, vcc
	global_load_dwordx4 v[96:99], v[98:99], off
	s_nop 0
	global_load_dwordx4 v[100:103], v[100:101], off
	s_waitcnt vmcnt(15)
	v_mul_f32_e32 v4, 0x42800000, v40
	v_mul_f32_e32 v40, 0x42800000, v41
	v_mul_f32_e32 v41, 0x42800000, v42
	v_mul_f32_e32 v42, 0x42800000, v43
	s_waitcnt vmcnt(14)
	v_mul_f32_e32 v43, 0x42800000, v44
	ds_write2_b32 v8, v4, v43 offset1:8
	v_mul_f32_e32 v4, 0x42800000, v45
	ds_write2_b32 v8, v40, v4 offset0:129 offset1:137
	v_mul_f32_e32 v4, 0x42800000, v46
	ds_write2_b32 v38, v41, v4 offset0:2 offset1:10
	v_mul_f32_e32 v4, 0x42800000, v47
	ds_write2_b32 v38, v42, v4 offset0:131 offset1:139
	s_waitcnt vmcnt(13)
	v_mul_f32_e32 v4, 0x42800000, v48
	s_waitcnt vmcnt(12)
	v_mul_f32_e32 v43, 0x42800000, v52
	v_mul_f32_e32 v40, 0x42800000, v49
	ds_write2_b32 v8, v4, v43 offset0:16 offset1:24
	v_mul_f32_e32 v4, 0x42800000, v53
	v_mul_f32_e32 v41, 0x42800000, v50
	ds_write2_b32 v8, v40, v4 offset0:145 offset1:153
	v_mul_f32_e32 v4, 0x42800000, v54
	v_mul_f32_e32 v42, 0x42800000, v51
	ds_write2_b32 v38, v41, v4 offset0:18 offset1:26
	v_mul_f32_e32 v4, 0x42800000, v55
	ds_write2_b32 v38, v42, v4 offset0:147 offset1:155
	s_waitcnt vmcnt(11)
	v_mul_f32_e32 v4, 0x42800000, v56
	s_waitcnt vmcnt(10)
	v_mul_f32_e32 v43, 0x42800000, v60
	v_mul_f32_e32 v40, 0x42800000, v57
	ds_write2_b32 v8, v4, v43 offset0:32 offset1:40
	v_mul_f32_e32 v4, 0x42800000, v61
	v_mul_f32_e32 v41, 0x42800000, v58
	ds_write2_b32 v8, v40, v4 offset0:161 offset1:169
	v_mul_f32_e32 v4, 0x42800000, v62
	v_mul_f32_e32 v42, 0x42800000, v59
	ds_write2_b32 v38, v41, v4 offset0:34 offset1:42
	v_mul_f32_e32 v4, 0x42800000, v63
	ds_write2_b32 v38, v42, v4 offset0:163 offset1:171
	s_waitcnt vmcnt(9)
	v_mul_f32_e32 v4, 0x42800000, v64
	s_waitcnt vmcnt(8)
	v_mul_f32_e32 v43, 0x42800000, v68
	v_mul_f32_e32 v40, 0x42800000, v65
	ds_write2_b32 v8, v4, v43 offset0:48 offset1:56
	v_mul_f32_e32 v4, 0x42800000, v69
	v_mul_f32_e32 v41, 0x42800000, v66
	ds_write2_b32 v8, v40, v4 offset0:177 offset1:185
	v_mul_f32_e32 v4, 0x42800000, v70
	v_mul_f32_e32 v42, 0x42800000, v67
	ds_write2_b32 v38, v41, v4 offset0:50 offset1:58
	v_mul_f32_e32 v4, 0x42800000, v71
	ds_write2_b32 v38, v42, v4 offset0:179 offset1:187
	s_waitcnt vmcnt(7)
	v_mul_f32_e32 v4, 0x42800000, v72
	s_waitcnt vmcnt(6)
	v_mul_f32_e32 v43, 0x42800000, v76
	v_mul_f32_e32 v40, 0x42800000, v73
	ds_write2_b32 v8, v4, v43 offset0:64 offset1:72
	v_mul_f32_e32 v4, 0x42800000, v77
	v_mul_f32_e32 v41, 0x42800000, v74
	ds_write2_b32 v8, v40, v4 offset0:193 offset1:201
	v_mul_f32_e32 v4, 0x42800000, v78
	v_mul_f32_e32 v42, 0x42800000, v75
	ds_write2_b32 v38, v41, v4 offset0:66 offset1:74
	v_mul_f32_e32 v4, 0x42800000, v79
	ds_write2_b32 v38, v42, v4 offset0:195 offset1:203
	s_waitcnt vmcnt(5)
	v_mul_f32_e32 v4, 0x42800000, v80
	s_waitcnt vmcnt(4)
	v_mul_f32_e32 v43, 0x42800000, v84
	v_mul_f32_e32 v40, 0x42800000, v81
	ds_write2_b32 v8, v4, v43 offset0:80 offset1:88
	v_mul_f32_e32 v4, 0x42800000, v85
	v_mul_f32_e32 v41, 0x42800000, v82
	ds_write2_b32 v8, v40, v4 offset0:209 offset1:217
	v_mul_f32_e32 v4, 0x42800000, v86
	v_mul_f32_e32 v42, 0x42800000, v83
	ds_write2_b32 v38, v41, v4 offset0:82 offset1:90
	v_mul_f32_e32 v4, 0x42800000, v87
	ds_write2_b32 v38, v42, v4 offset0:211 offset1:219
	s_waitcnt vmcnt(3)
	v_mul_f32_e32 v4, 0x42800000, v88
	s_waitcnt vmcnt(2)
	v_mul_f32_e32 v43, 0x42800000, v92
	v_mul_f32_e32 v40, 0x42800000, v89
	ds_write2_b32 v8, v4, v43 offset0:96 offset1:104
	v_mul_f32_e32 v4, 0x42800000, v93
	v_mul_f32_e32 v41, 0x42800000, v90
	ds_write2_b32 v8, v40, v4 offset0:225 offset1:233
	v_mul_f32_e32 v4, 0x42800000, v94
	v_mul_f32_e32 v42, 0x42800000, v91
	ds_write2_b32 v38, v41, v4 offset0:98 offset1:106
	v_mul_f32_e32 v4, 0x42800000, v95
	ds_write2_b32 v38, v42, v4 offset0:227 offset1:235
	s_waitcnt vmcnt(1)
	v_mul_f32_e32 v4, 0x42800000, v96
	s_waitcnt vmcnt(0)
	v_mul_f32_e32 v43, 0x42800000, v100
	v_mul_f32_e32 v40, 0x42800000, v97
	ds_write2_b32 v8, v4, v43 offset0:112 offset1:120
	v_mul_f32_e32 v4, 0x42800000, v101
	v_mul_f32_e32 v41, 0x42800000, v98
	ds_write2_b32 v8, v40, v4 offset0:241 offset1:249
	v_mul_f32_e32 v4, 0x42800000, v102
	v_mul_f32_e32 v42, 0x42800000, v99
	ds_write2_b32 v38, v41, v4 offset0:114 offset1:122
	v_mul_f32_e32 v4, 0x42800000, v103
	ds_write2_b32 v38, v42, v4 offset0:243 offset1:251
	s_waitcnt lgkmcnt(0)
	ds_read2_b32 v[40:41], v13 offset1:1
	ds_read2_b32 v[42:43], v13 offset0:2 offset1:3
	ds_read2_b32 v[44:45], v13 offset0:4 offset1:5
	ds_read2_b32 v[46:47], v13 offset0:6 offset1:7
	v_lshl_add_u64 v[48:49], s[6:7], 0, v[2:3]
	v_readlane_b32 s70, v255, 13
	v_readlane_b32 s71, v255, 14
	s_waitcnt lgkmcnt(3)
	v_med3_f32 v4, v40, s34, v39
	v_med3_f32 v41, v41, s34, v39
	v_mov_b32_e32 v40, v5
	v_cvt_pk_fp8_f32 v40, v4, v41
	s_waitcnt lgkmcnt(2)
	v_med3_f32 v4, v42, s34, v39
	v_med3_f32 v41, v43, s34, v39
	s_waitcnt lgkmcnt(1)
	v_med3_f32 v42, v45, s34, v39
	v_cvt_pk_fp8_f32 v40, v4, v41 op_sel:[0,0,1]
	v_med3_f32 v4, v44, s34, v39
	v_mov_b32_e32 v41, v5
	v_cvt_pk_fp8_f32 v41, v4, v42
	ds_read2_b32 v[42:43], v13 offset0:8 offset1:9
	s_waitcnt lgkmcnt(1)
	v_med3_f32 v4, v46, s34, v39
	v_med3_f32 v44, v47, s34, v39
	v_cvt_pk_fp8_f32 v41, v4, v44 op_sel:[0,0,1]
	ds_read2_b32 v[44:45], v13 offset0:10 offset1:11
	ds_read2_b32 v[46:47], v13 offset0:12 offset1:13
	ds_read2_b32 v[50:51], v13 offset0:14 offset1:15
	s_waitcnt lgkmcnt(3)
	v_med3_f32 v4, v42, s34, v39
	v_med3_f32 v43, v43, s34, v39
	v_mov_b32_e32 v42, v5
	v_cvt_pk_fp8_f32 v42, v4, v43
	s_waitcnt lgkmcnt(2)
	v_med3_f32 v4, v44, s34, v39
	v_med3_f32 v44, v45, s34, v39
	s_waitcnt lgkmcnt(1)
	v_med3_f32 v45, v46, s34, v39
	v_med3_f32 v46, v47, s34, v39
	v_mov_b32_e32 v43, v5
	v_cvt_pk_fp8_f32 v43, v45, v46
	v_cvt_pk_fp8_f32 v42, v4, v44 op_sel:[0,0,1]
	s_waitcnt lgkmcnt(0)
	v_med3_f32 v4, v50, s34, v39
	v_med3_f32 v44, v51, s34, v39
	v_cvt_pk_fp8_f32 v43, v4, v44 op_sel:[0,0,1]
	ds_read2_b32 v[44:45], v14 offset1:1
	v_or_b32_e32 v4, s2, v1
	v_lshlrev_b32_e32 v4, 10, v4
	v_lshl_add_u64 v[46:47], v[48:49], 0, v[4:5]
	ds_read2_b32 v[50:51], v15 offset1:1
	ds_read2_b32 v[52:53], v16 offset1:1
	ds_read2_b32 v[54:55], v17 offset1:1
	s_waitcnt lgkmcnt(3)
	v_med3_f32 v4, v44, s34, v39
	v_med3_f32 v45, v45, s34, v39
	v_mov_b32_e32 v44, v5
	v_cvt_pk_fp8_f32 v44, v4, v45
	global_store_dwordx4 v[46:47], v[40:43], off nt
	s_waitcnt lgkmcnt(2)
	v_med3_f32 v4, v50, s34, v39
	v_mov_b32_e32 v45, v5
	v_med3_f32 v40, v51, s34, v39
	v_cvt_pk_fp8_f32 v44, v4, v40 op_sel:[0,0,1]
	s_waitcnt lgkmcnt(1)
	v_med3_f32 v4, v52, s34, v39
	v_med3_f32 v40, v53, s34, v39
	v_cvt_pk_fp8_f32 v45, v4, v40
	ds_read2_b32 v[40:41], v18 offset1:1
	s_waitcnt lgkmcnt(1)
	v_med3_f32 v4, v54, s34, v39
	v_med3_f32 v42, v55, s34, v39
	v_cvt_pk_fp8_f32 v45, v4, v42 op_sel:[0,0,1]
	ds_read2_b32 v[42:43], v19 offset1:1
	ds_read2_b32 v[50:51], v20 offset1:1
	ds_read2_b32 v[52:53], v21 offset1:1
	s_waitcnt lgkmcnt(3)
	v_med3_f32 v4, v40, s34, v39
	v_med3_f32 v40, v41, s34, v39
	v_mov_b32_e32 v46, v5
	v_cvt_pk_fp8_f32 v46, v4, v40
	s_waitcnt lgkmcnt(2)
	v_med3_f32 v4, v42, s34, v39
	s_waitcnt lgkmcnt(1)
	v_med3_f32 v41, v50, s34, v39
	v_med3_f32 v42, v51, s34, v39
	v_mov_b32_e32 v47, v5
	v_cvt_pk_fp8_f32 v47, v41, v42
	v_med3_f32 v40, v43, s34, v39
	v_cvt_pk_fp8_f32 v46, v4, v40 op_sel:[0,0,1]
	s_waitcnt lgkmcnt(0)
	v_med3_f32 v4, v52, s34, v39
	v_med3_f32 v40, v53, s34, v39
	v_cvt_pk_fp8_f32 v47, v4, v40 op_sel:[0,0,1]
	ds_read2_b32 v[40:41], v22 offset1:1
	v_or_b32_e32 v4, s2, v9
	v_lshlrev_b32_e32 v4, 10, v4
	v_lshl_add_u64 v[42:43], v[48:49], 0, v[4:5]
	ds_read2_b32 v[50:51], v23 offset1:1
	ds_read2_b32 v[52:53], v24 offset1:1
	ds_read2_b32 v[54:55], v25 offset1:1
	s_waitcnt lgkmcnt(3)
	v_med3_f32 v4, v40, s34, v39
	v_med3_f32 v41, v41, s34, v39
	v_mov_b32_e32 v40, v5
	v_cvt_pk_fp8_f32 v40, v4, v41
	s_waitcnt lgkmcnt(2)
	v_med3_f32 v4, v50, s34, v39
	v_med3_f32 v41, v51, s34, v39
	global_store_dwordx4 v[42:43], v[44:47], off nt
	v_cvt_pk_fp8_f32 v40, v4, v41 op_sel:[0,0,1]
	s_waitcnt lgkmcnt(1)
	v_med3_f32 v4, v52, s34, v39
	v_med3_f32 v42, v53, s34, v39
	v_mov_b32_e32 v41, v5
	v_cvt_pk_fp8_f32 v41, v4, v42
	ds_read2_b32 v[42:43], v26 offset1:1
	s_waitcnt lgkmcnt(1)
	v_med3_f32 v4, v54, s34, v39
	v_med3_f32 v44, v55, s34, v39
	v_cvt_pk_fp8_f32 v41, v4, v44 op_sel:[0,0,1]
	ds_read2_b32 v[44:45], v27 offset1:1
	ds_read2_b32 v[46:47], v28 offset1:1
	ds_read2_b32 v[50:51], v29 offset1:1
	s_waitcnt lgkmcnt(3)
	v_med3_f32 v4, v42, s34, v39
	v_med3_f32 v43, v43, s34, v39
	v_mov_b32_e32 v42, v5
	v_cvt_pk_fp8_f32 v42, v4, v43
	s_waitcnt lgkmcnt(2)
	v_med3_f32 v4, v44, s34, v39
	v_med3_f32 v44, v45, s34, v39
	s_waitcnt lgkmcnt(1)
	v_med3_f32 v45, v46, s34, v39
	v_med3_f32 v46, v47, s34, v39
	v_mov_b32_e32 v43, v5
	v_cvt_pk_fp8_f32 v43, v45, v46
	v_cvt_pk_fp8_f32 v42, v4, v44 op_sel:[0,0,1]
	s_waitcnt lgkmcnt(0)
	v_med3_f32 v4, v50, s34, v39
	v_med3_f32 v44, v51, s34, v39
	v_cvt_pk_fp8_f32 v43, v4, v44 op_sel:[0,0,1]
	ds_read2_b32 v[44:45], v30 offset1:1
	v_or_b32_e32 v4, s2, v10
	v_lshlrev_b32_e32 v4, 10, v4
	v_lshl_add_u64 v[46:47], v[48:49], 0, v[4:5]
	ds_read2_b32 v[50:51], v31 offset1:1
	ds_read2_b32 v[52:53], v32 offset1:1
	ds_read2_b32 v[54:55], v33 offset1:1
	s_waitcnt lgkmcnt(3)
	v_med3_f32 v4, v44, s34, v39
	v_med3_f32 v45, v45, s34, v39
	v_mov_b32_e32 v44, v5
	v_cvt_pk_fp8_f32 v44, v4, v45
	global_store_dwordx4 v[46:47], v[40:43], off nt
	s_waitcnt lgkmcnt(2)
	v_med3_f32 v4, v50, s34, v39
	v_mov_b32_e32 v45, v5
	v_med3_f32 v40, v51, s34, v39
	v_cvt_pk_fp8_f32 v44, v4, v40 op_sel:[0,0,1]
	s_waitcnt lgkmcnt(1)
	v_med3_f32 v4, v52, s34, v39
	v_med3_f32 v40, v53, s34, v39
	v_cvt_pk_fp8_f32 v45, v4, v40
	ds_read2_b32 v[40:41], v34 offset1:1
	s_waitcnt lgkmcnt(1)
	v_med3_f32 v4, v54, s34, v39
	v_med3_f32 v42, v55, s34, v39
	v_cvt_pk_fp8_f32 v45, v4, v42 op_sel:[0,0,1]
	ds_read2_b32 v[42:43], v35 offset1:1
	ds_read2_b32 v[50:51], v36 offset1:1
	ds_read2_b32 v[52:53], v37 offset1:1
	s_waitcnt lgkmcnt(3)
	v_med3_f32 v4, v40, s34, v39
	v_med3_f32 v40, v41, s34, v39
	v_mov_b32_e32 v46, v5
	v_cvt_pk_fp8_f32 v46, v4, v40
	s_waitcnt lgkmcnt(2)
	v_med3_f32 v4, v42, s34, v39
	s_waitcnt lgkmcnt(1)
	v_med3_f32 v41, v50, s34, v39
	v_med3_f32 v42, v51, s34, v39
	v_mov_b32_e32 v47, v5
	v_cvt_pk_fp8_f32 v47, v41, v42
	v_med3_f32 v40, v43, s34, v39
	v_cvt_pk_fp8_f32 v46, v4, v40 op_sel:[0,0,1]
	s_waitcnt lgkmcnt(0)
	v_med3_f32 v4, v52, s34, v39
	v_med3_f32 v40, v53, s34, v39
	v_cvt_pk_fp8_f32 v47, v4, v40 op_sel:[0,0,1]
	v_or_b32_e32 v4, s2, v11
	v_lshlrev_b32_e32 v4, 10, v4
	v_lshl_add_u64 v[40:41], v[48:49], 0, v[4:5]
	global_store_dwordx4 v[40:41], v[44:47], off nt
	s_waitcnt lgkmcnt(0)
	s_mov_b64 s[54:55], s[74:75]
	s_branch .LBB0_619

.LBB0_693:
	s_or_b64 exec, exec, s[4:5]
	s_waitcnt lgkmcnt(0)
	s_barrier
	ds_read_b32 v4, v11
	s_mov_b64 s[4:5], -1
	s_waitcnt lgkmcnt(0)
	v_cmp_lt_u32_e32 vcc, s15, v4
	v_readfirstlane_b32 s2, v4
	s_cbranch_vccnz .LBB0_688
	s_lshl_b32 s6, s2, 3
	s_add_i32 s6, s6, s91
	s_cmpk_gt_u32 s6, 0x5fff
	s_cbranch_scc1 .LBB0_687
	s_lshl_b32 s7, s6, 5
	s_cmpk_gt_u32 s6, 0x3fff
	s_cbranch_scc0 .LBB0_697
	s_add_i32 s2, s6, 0xffffc000
	s_lshr_b32 s2, s2, 8
	s_lshl_b64 s[4:5], s[2:3], 20
	s_lshl_b64 s[8:9], s[2:3], 22
	s_add_u32 s8, s76, s8
	s_addc_u32 s9, s77, s9
	s_add_u32 s4, s10, s4
	s_addc_u32 s5, s11, s5
	s_lshl_b32 s2, s6, 2
	s_and_b32 s43, s2, 0x380
	s_and_b32 s2, s7, 0x3e0
	v_or_b32_e32 v4, s2, v6
	v_or_b32_e32 v39, s43, v1
	v_lshlrev_b32_e32 v4, 2, v4
	v_lshl_add_u64 v[40:41], s[8:9], 0, v[4:5]
	v_lshlrev_b32_e32 v4, 12, v39
	v_lshl_add_u64 v[96:97], v[40:41], 0, v[4:5]
	v_add_co_u32_e32 v44, vcc, s16, v96
	global_load_dwordx4 v[40:43], v[96:97], off
	s_nop 0
	v_addc_co_u32_e32 v45, vcc, 0, v97, vcc
	global_load_dwordx4 v[44:47], v[44:45], off
	v_add_co_u32_e32 v48, vcc, s17, v96
	s_add_u32 s4, s4, s43
	s_nop 0
	v_addc_co_u32_e32 v49, vcc, 0, v97, vcc
	v_add_co_u32_e32 v52, vcc, s18, v96
	global_load_dwordx4 v[48:51], v[48:49], off
	s_nop 0
	v_addc_co_u32_e32 v53, vcc, 0, v97, vcc
	global_load_dwordx4 v[52:55], v[52:53], off
	v_add_co_u32_e32 v56, vcc, s19, v96
	s_addc_u32 s5, s5, 0
	s_nop 0
	v_addc_co_u32_e32 v57, vcc, 0, v97, vcc
	v_add_co_u32_e32 v60, vcc, s20, v96
	global_load_dwordx4 v[56:59], v[56:57], off
	s_nop 0
	v_addc_co_u32_e32 v61, vcc, 0, v97, vcc
	global_load_dwordx4 v[60:63], v[60:61], off
	v_add_co_u32_e32 v64, vcc, s21, v96
	s_nop 1
	v_addc_co_u32_e32 v65, vcc, 0, v97, vcc
	v_add_co_u32_e32 v68, vcc, s22, v96
	global_load_dwordx4 v[64:67], v[64:65], off
	s_nop 0
	v_addc_co_u32_e32 v69, vcc, 0, v97, vcc
	global_load_dwordx4 v[68:71], v[68:69], off
	v_add_co_u32_e32 v72, vcc, s23, v96
	s_waitcnt vmcnt(7)
	v_mul_f32_e32 v4, 0x42800000, v40
	v_addc_co_u32_e32 v73, vcc, 0, v97, vcc
	v_add_co_u32_e32 v76, vcc, s24, v96
	v_mul_f32_e32 v40, 0x42800000, v42
	s_nop 0
	v_addc_co_u32_e32 v77, vcc, 0, v97, vcc
	global_load_dwordx4 v[72:75], v[72:73], off
	s_nop 0
	global_load_dwordx4 v[76:79], v[76:77], off
	v_add_co_u32_e32 v80, vcc, s25, v96
	s_waitcnt vmcnt(8)
	v_mul_f32_e32 v42, 0x42800000, v44
	v_addc_co_u32_e32 v81, vcc, 0, v97, vcc
	v_add_co_u32_e32 v84, vcc, s26, v96
	v_mul_f32_e32 v39, 0x42800000, v41
	s_nop 0
	v_addc_co_u32_e32 v85, vcc, 0, v97, vcc
	global_load_dwordx4 v[80:83], v[80:81], off
	s_nop 0
	global_load_dwordx4 v[84:87], v[84:85], off
	v_add_co_u32_e32 v88, vcc, s27, v96
	v_mul_f32_e32 v41, 0x42800000, v43
	s_nop 0
	v_addc_co_u32_e32 v89, vcc, 0, v97, vcc
	v_add_co_u32_e32 v92, vcc, s28, v96
	s_nop 1
	v_addc_co_u32_e32 v93, vcc, 0, v97, vcc
	global_load_dwordx4 v[88:91], v[88:89], off
	s_nop 0
	global_load_dwordx4 v[92:95], v[92:93], off
	v_add_co_u32_e32 v98, vcc, s29, v96
	s_nop 1
	v_addc_co_u32_e32 v99, vcc, 0, v97, vcc
	v_add_co_u32_e32 v100, vcc, s30, v96
	s_nop 1
	v_addc_co_u32_e32 v101, vcc, 0, v97, vcc
	global_load_dwordx4 v[96:99], v[98:99], off
	s_nop 0
	global_load_dwordx4 v[100:103], v[100:101], off
	ds_write2_b32 v7, v4, v42 offset1:8
	v_mul_f32_e32 v4, 0x42800000, v45
	ds_write2_b32 v7, v39, v4 offset0:129 offset1:137
	v_mul_f32_e32 v4, 0x42800000, v46
	ds_write2_b32 v37, v40, v4 offset0:2 offset1:10
	v_mul_f32_e32 v4, 0x42800000, v47
	ds_write2_b32 v37, v41, v4 offset0:131 offset1:139
	s_waitcnt vmcnt(13)
	v_mul_f32_e32 v4, 0x42800000, v48
	s_waitcnt vmcnt(12)
	v_mul_f32_e32 v42, 0x42800000, v52
	v_mul_f32_e32 v39, 0x42800000, v49
	ds_write2_b32 v7, v4, v42 offset0:16 offset1:24
	v_mul_f32_e32 v4, 0x42800000, v53
	v_mul_f32_e32 v40, 0x42800000, v50
	ds_write2_b32 v7, v39, v4 offset0:145 offset1:153
	v_mul_f32_e32 v4, 0x42800000, v54
	v_mul_f32_e32 v41, 0x42800000, v51
	ds_write2_b32 v37, v40, v4 offset0:18 offset1:26
	v_mul_f32_e32 v4, 0x42800000, v55
	ds_write2_b32 v37, v41, v4 offset0:147 offset1:155
	s_waitcnt vmcnt(11)
	v_mul_f32_e32 v4, 0x42800000, v56
	s_waitcnt vmcnt(10)
	v_mul_f32_e32 v42, 0x42800000, v60
	v_mul_f32_e32 v39, 0x42800000, v57
	ds_write2_b32 v7, v4, v42 offset0:32 offset1:40
	v_mul_f32_e32 v4, 0x42800000, v61
	v_mul_f32_e32 v40, 0x42800000, v58
	ds_write2_b32 v7, v39, v4 offset0:161 offset1:169
	v_mul_f32_e32 v4, 0x42800000, v62
	v_mul_f32_e32 v41, 0x42800000, v59
	ds_write2_b32 v37, v40, v4 offset0:34 offset1:42
	v_mul_f32_e32 v4, 0x42800000, v63
	ds_write2_b32 v37, v41, v4 offset0:163 offset1:171
	s_waitcnt vmcnt(9)
	v_mul_f32_e32 v4, 0x42800000, v64
	s_waitcnt vmcnt(8)
	v_mul_f32_e32 v42, 0x42800000, v68
	v_mul_f32_e32 v39, 0x42800000, v65
	ds_write2_b32 v7, v4, v42 offset0:48 offset1:56
	v_mul_f32_e32 v4, 0x42800000, v69
	v_mul_f32_e32 v40, 0x42800000, v66
	ds_write2_b32 v7, v39, v4 offset0:177 offset1:185
	v_mul_f32_e32 v4, 0x42800000, v70
	v_mul_f32_e32 v41, 0x42800000, v67
	ds_write2_b32 v37, v40, v4 offset0:50 offset1:58
	v_mul_f32_e32 v4, 0x42800000, v71
	ds_write2_b32 v37, v41, v4 offset0:179 offset1:187
	v_lshl_add_u64 v[48:49], s[4:5], 0, v[2:3]
	s_mov_b64 s[4:5], 0
	s_waitcnt vmcnt(7)
	v_mul_f32_e32 v4, 0x42800000, v72
	s_waitcnt vmcnt(6)
	v_mul_f32_e32 v42, 0x42800000, v76
	v_mul_f32_e32 v39, 0x42800000, v73
	ds_write2_b32 v7, v4, v42 offset0:64 offset1:72
	v_mul_f32_e32 v4, 0x42800000, v77
	v_mul_f32_e32 v40, 0x42800000, v74
	ds_write2_b32 v7, v39, v4 offset0:193 offset1:201
	v_mul_f32_e32 v4, 0x42800000, v78
	v_mul_f32_e32 v41, 0x42800000, v75
	ds_write2_b32 v37, v40, v4 offset0:66 offset1:74
	v_mul_f32_e32 v4, 0x42800000, v79
	ds_write2_b32 v37, v41, v4 offset0:195 offset1:203
	s_waitcnt vmcnt(5)
	v_mul_f32_e32 v4, 0x42800000, v80
	s_waitcnt vmcnt(4)
	v_mul_f32_e32 v42, 0x42800000, v84
	v_mul_f32_e32 v39, 0x42800000, v81
	ds_write2_b32 v7, v4, v42 offset0:80 offset1:88
	v_mul_f32_e32 v4, 0x42800000, v85
	v_mul_f32_e32 v40, 0x42800000, v82
	ds_write2_b32 v7, v39, v4 offset0:209 offset1:217
	v_mul_f32_e32 v4, 0x42800000, v86
	v_mul_f32_e32 v41, 0x42800000, v83
	ds_write2_b32 v37, v40, v4 offset0:82 offset1:90
	v_mul_f32_e32 v4, 0x42800000, v87
	ds_write2_b32 v37, v41, v4 offset0:211 offset1:219
	s_waitcnt vmcnt(3)
	v_mul_f32_e32 v4, 0x42800000, v88
	s_waitcnt vmcnt(2)
	v_mul_f32_e32 v42, 0x42800000, v92
	v_mul_f32_e32 v39, 0x42800000, v89
	ds_write2_b32 v7, v4, v42 offset0:96 offset1:104
	v_mul_f32_e32 v4, 0x42800000, v93
	v_mul_f32_e32 v40, 0x42800000, v90
	ds_write2_b32 v7, v39, v4 offset0:225 offset1:233
	v_mul_f32_e32 v4, 0x42800000, v94
	v_mul_f32_e32 v41, 0x42800000, v91
	ds_write2_b32 v37, v40, v4 offset0:98 offset1:106
	v_mul_f32_e32 v4, 0x42800000, v95
	ds_write2_b32 v37, v41, v4 offset0:227 offset1:235
	s_waitcnt vmcnt(1)
	v_mul_f32_e32 v4, 0x42800000, v96
	s_waitcnt vmcnt(0)
	v_mul_f32_e32 v42, 0x42800000, v100
	v_mul_f32_e32 v39, 0x42800000, v97
	ds_write2_b32 v7, v4, v42 offset0:112 offset1:120
	v_mul_f32_e32 v4, 0x42800000, v101
	v_mul_f32_e32 v40, 0x42800000, v98
	ds_write2_b32 v7, v39, v4 offset0:241 offset1:249
	v_mul_f32_e32 v4, 0x42800000, v102
	v_mul_f32_e32 v41, 0x42800000, v99
	ds_write2_b32 v37, v40, v4 offset0:114 offset1:122
	v_mul_f32_e32 v4, 0x42800000, v103
	ds_write2_b32 v37, v41, v4 offset0:243 offset1:251
	s_waitcnt lgkmcnt(0)
	ds_read2_b32 v[40:41], v12 offset1:1
	ds_read2_b32 v[42:43], v12 offset0:2 offset1:3
	ds_read2_b32 v[44:45], v12 offset0:4 offset1:5
	ds_read2_b32 v[46:47], v12 offset0:6 offset1:7
	s_waitcnt lgkmcnt(3)
	v_med3_f32 v4, v40, s31, v38
	v_med3_f32 v39, v41, s31, v38
	v_mov_b32_e32 v40, v5
	v_cvt_pk_fp8_f32 v40, v4, v39
	s_waitcnt lgkmcnt(2)
	v_med3_f32 v4, v42, s31, v38
	v_med3_f32 v39, v43, s31, v38
	v_mov_b32_e32 v41, v5
	v_cvt_pk_fp8_f32 v40, v4, v39 op_sel:[0,0,1]
	s_waitcnt lgkmcnt(1)
	v_med3_f32 v4, v44, s31, v38
	v_med3_f32 v39, v45, s31, v38
	ds_read2_b32 v[42:43], v12 offset0:8 offset1:9
	v_cvt_pk_fp8_f32 v41, v4, v39
	s_waitcnt lgkmcnt(1)
	v_med3_f32 v4, v46, s31, v38
	v_med3_f32 v39, v47, s31, v38
	ds_read2_b32 v[44:45], v12 offset0:10 offset1:11
	ds_read2_b32 v[46:47], v12 offset0:12 offset1:13
	ds_read2_b32 v[50:51], v12 offset0:14 offset1:15
	v_cvt_pk_fp8_f32 v41, v4, v39 op_sel:[0,0,1]
	s_waitcnt lgkmcnt(3)
	v_med3_f32 v4, v42, s31, v38
	v_med3_f32 v39, v43, s31, v38
	v_mov_b32_e32 v42, v5
	v_cvt_pk_fp8_f32 v42, v4, v39
	s_waitcnt lgkmcnt(2)
	v_med3_f32 v4, v44, s31, v38
	v_med3_f32 v39, v45, s31, v38
	s_waitcnt lgkmcnt(1)
	v_med3_f32 v44, v46, s31, v38
	v_med3_f32 v45, v47, s31, v38
	v_mov_b32_e32 v43, v5
	v_cvt_pk_fp8_f32 v43, v44, v45
	ds_read2_b32 v[44:45], v13 offset1:1
	v_cvt_pk_fp8_f32 v42, v4, v39 op_sel:[0,0,1]
	s_waitcnt lgkmcnt(1)
	v_med3_f32 v4, v50, s31, v38
	v_med3_f32 v39, v51, s31, v38
	v_cvt_pk_fp8_f32 v43, v4, v39 op_sel:[0,0,1]
	v_or_b32_e32 v4, s2, v1
	v_lshlrev_b32_e32 v4, 10, v4
	v_lshl_add_u64 v[46:47], v[48:49], 0, v[4:5]
	s_waitcnt lgkmcnt(0)
	v_med3_f32 v4, v44, s31, v38
	v_med3_f32 v39, v45, s31, v38
	v_mov_b32_e32 v44, v5
	ds_read2_b32 v[50:51], v14 offset1:1
	ds_read2_b32 v[52:53], v15 offset1:1
	ds_read2_b32 v[54:55], v16 offset1:1
	v_cvt_pk_fp8_f32 v44, v4, v39
	global_store_dwordx4 v[46:47], v[40:43], off nt
	s_waitcnt lgkmcnt(2)
	v_med3_f32 v4, v50, s31, v38
	v_med3_f32 v39, v51, s31, v38
	v_cvt_pk_fp8_f32 v44, v4, v39 op_sel:[0,0,1]
	s_waitcnt lgkmcnt(1)
	v_med3_f32 v4, v52, s31, v38
	v_med3_f32 v39, v53, s31, v38
	v_mov_b32_e32 v45, v5
	ds_read2_b32 v[40:41], v17 offset1:1
	v_cvt_pk_fp8_f32 v45, v4, v39
	ds_read2_b32 v[42:43], v18 offset1:1
	ds_read2_b32 v[50:51], v19 offset1:1
	ds_read2_b32 v[52:53], v20 offset1:1
	s_waitcnt lgkmcnt(4)
	v_med3_f32 v4, v54, s31, v38
	v_med3_f32 v39, v55, s31, v38
	v_cvt_pk_fp8_f32 v45, v4, v39 op_sel:[0,0,1]
	s_waitcnt lgkmcnt(3)
	v_med3_f32 v4, v40, s31, v38
	v_med3_f32 v39, v41, s31, v38
	v_mov_b32_e32 v46, v5
	v_cvt_pk_fp8_f32 v46, v4, v39
	s_waitcnt lgkmcnt(1)
	v_med3_f32 v40, v50, s31, v38
	v_med3_f32 v41, v51, s31, v38
	v_mov_b32_e32 v47, v5
	v_cvt_pk_fp8_f32 v47, v40, v41
	ds_read2_b32 v[40:41], v21 offset1:1
	v_med3_f32 v4, v42, s31, v38
	v_med3_f32 v39, v43, s31, v38
	v_cvt_pk_fp8_f32 v46, v4, v39 op_sel:[0,0,1]
	s_waitcnt lgkmcnt(1)
	v_med3_f32 v4, v52, s31, v38
	v_med3_f32 v39, v53, s31, v38
	v_cvt_pk_fp8_f32 v47, v4, v39 op_sel:[0,0,1]
	v_or_b32_e32 v4, s2, v8
	v_lshlrev_b32_e32 v4, 10, v4
	v_lshl_add_u64 v[42:43], v[48:49], 0, v[4:5]
	s_waitcnt lgkmcnt(0)
	v_med3_f32 v4, v40, s31, v38
	v_med3_f32 v39, v41, s31, v38
	v_mov_b32_e32 v40, v5
	ds_read2_b32 v[50:51], v22 offset1:1
	ds_read2_b32 v[52:53], v23 offset1:1
	ds_read2_b32 v[54:55], v24 offset1:1
	v_cvt_pk_fp8_f32 v40, v4, v39
	global_store_dwordx4 v[42:43], v[44:47], off nt
	s_waitcnt lgkmcnt(2)
	v_med3_f32 v4, v50, s31, v38
	v_med3_f32 v39, v51, s31, v38
	v_cvt_pk_fp8_f32 v40, v4, v39 op_sel:[0,0,1]
	s_waitcnt lgkmcnt(1)
	v_med3_f32 v4, v52, s31, v38
	v_med3_f32 v39, v53, s31, v38
	v_mov_b32_e32 v41, v5
	ds_read2_b32 v[42:43], v25 offset1:1
	v_cvt_pk_fp8_f32 v41, v4, v39
	ds_read2_b32 v[44:45], v26 offset1:1
	ds_read2_b32 v[46:47], v27 offset1:1
	ds_read2_b32 v[50:51], v28 offset1:1
	s_waitcnt lgkmcnt(4)
	v_med3_f32 v4, v54, s31, v38
	v_med3_f32 v39, v55, s31, v38
	v_cvt_pk_fp8_f32 v41, v4, v39 op_sel:[0,0,1]
	s_waitcnt lgkmcnt(3)
	v_med3_f32 v4, v42, s31, v38
	v_med3_f32 v39, v43, s31, v38
	v_mov_b32_e32 v42, v5
	v_cvt_pk_fp8_f32 v42, v4, v39
	s_waitcnt lgkmcnt(2)
	v_med3_f32 v4, v44, s31, v38
	v_med3_f32 v39, v45, s31, v38
	s_waitcnt lgkmcnt(1)
	v_med3_f32 v44, v46, s31, v38
	v_med3_f32 v45, v47, s31, v38
	v_mov_b32_e32 v43, v5
	v_cvt_pk_fp8_f32 v43, v44, v45
	ds_read2_b32 v[44:45], v29 offset1:1
	v_cvt_pk_fp8_f32 v42, v4, v39 op_sel:[0,0,1]
	s_waitcnt lgkmcnt(1)
	v_med3_f32 v4, v50, s31, v38
	v_med3_f32 v39, v51, s31, v38
	v_cvt_pk_fp8_f32 v43, v4, v39 op_sel:[0,0,1]
	v_or_b32_e32 v4, s2, v9
	v_lshlrev_b32_e32 v4, 10, v4
	v_lshl_add_u64 v[46:47], v[48:49], 0, v[4:5]
	s_waitcnt lgkmcnt(0)
	v_med3_f32 v4, v44, s31, v38
	v_med3_f32 v39, v45, s31, v38
	v_mov_b32_e32 v44, v5
	ds_read2_b32 v[50:51], v30 offset1:1
	ds_read2_b32 v[52:53], v31 offset1:1
	ds_read2_b32 v[54:55], v32 offset1:1
	v_cvt_pk_fp8_f32 v44, v4, v39
	global_store_dwordx4 v[46:47], v[40:43], off nt
	s_waitcnt lgkmcnt(2)
	v_med3_f32 v4, v50, s31, v38
	v_med3_f32 v39, v51, s31, v38
	v_cvt_pk_fp8_f32 v44, v4, v39 op_sel:[0,0,1]
	s_waitcnt lgkmcnt(1)
	v_med3_f32 v4, v52, s31, v38
	v_med3_f32 v39, v53, s31, v38
	v_mov_b32_e32 v45, v5
	ds_read2_b32 v[40:41], v33 offset1:1
	v_cvt_pk_fp8_f32 v45, v4, v39
	ds_read2_b32 v[42:43], v34 offset1:1
	ds_read2_b32 v[50:51], v35 offset1:1
	ds_read2_b32 v[52:53], v36 offset1:1
	s_waitcnt lgkmcnt(4)
	v_med3_f32 v4, v54, s31, v38
	v_med3_f32 v39, v55, s31, v38
	v_cvt_pk_fp8_f32 v45, v4, v39 op_sel:[0,0,1]
	s_waitcnt lgkmcnt(3)
	v_med3_f32 v4, v40, s31, v38
	v_med3_f32 v39, v41, s31, v38
	v_mov_b32_e32 v46, v5
	v_cvt_pk_fp8_f32 v46, v4, v39
	s_waitcnt lgkmcnt(1)
	v_med3_f32 v40, v50, s31, v38
	v_med3_f32 v41, v51, s31, v38
	v_mov_b32_e32 v47, v5
	v_cvt_pk_fp8_f32 v47, v40, v41
	v_med3_f32 v4, v42, s31, v38
	v_med3_f32 v39, v43, s31, v38
	v_cvt_pk_fp8_f32 v46, v4, v39 op_sel:[0,0,1]
	s_waitcnt lgkmcnt(0)
	v_med3_f32 v4, v52, s31, v38
	v_med3_f32 v39, v53, s31, v38
	v_cvt_pk_fp8_f32 v47, v4, v39 op_sel:[0,0,1]
	v_or_b32_e32 v4, s2, v10
	v_lshlrev_b32_e32 v4, 10, v4
	v_lshl_add_u64 v[40:41], v[48:49], 0, v[4:5]
	global_store_dwordx4 v[40:41], v[44:47], off nt
	s_waitcnt lgkmcnt(0)
.LBB0_697:
	s_andn2_b64 vcc, exec, s[4:5]
	s_cbranch_vccnz .LBB0_687
	v_readlane_b32 s60, v255, 3
	s_lshr_b32 s2, s6, 9
	v_readlane_b32 s72, v255, 15
	v_readlane_b32 s73, v255, 16
	s_lshl_b64 s[4:5], s[2:3], 23
	v_readlane_b32 s74, v255, 17
	v_readlane_b32 s75, v255, 18
	s_mov_b64 s[52:53], s[72:73]
	s_add_u32 s44, s52, s4
	s_addc_u32 s45, s53, s5
	s_lshl_b64 s[8:9], s[2:3], 21
	s_add_u32 s5, s12, s8
	s_addc_u32 s4, s13, s9
	s_lshl_b32 s2, s6, 1
	s_and_b32 s8, s2, 0x380
	s_and_b32 s2, s7, 0x7e0
	s_and_b32 s7, s7, 0xe0
	s_cmpk_lt_u32 s7, 0x80
	s_cselect_b64 vcc, -1, 0
	s_lshl_b32 s6, s6, 4
	v_or_b32_e32 v4, s7, v6
	s_and_b32 s6, s6, 0x380
	v_or_b32_e32 v39, s6, v4
	s_addk_i32 s6, 0x380
	v_add_u32_e32 v4, s6, v4
	v_cndmask_b32_e32 v4, v4, v39, vcc
	v_or_b32_e32 v39, s8, v1
	v_lshlrev_b32_e32 v4, 2, v4
	v_lshl_add_u64 v[40:41], s[44:45], 0, v[4:5]
	v_lshlrev_b32_e32 v4, 13, v39
	v_lshl_add_u64 v[96:97], v[40:41], 0, v[4:5]
	v_add_co_u32_e32 v44, vcc, s17, v96
	global_load_dwordx4 v[40:43], v[96:97], off
	s_nop 0
	v_addc_co_u32_e32 v45, vcc, 0, v97, vcc
	global_load_dwordx4 v[44:47], v[44:45], off
	v_add_co_u32_e32 v48, vcc, s19, v96
	s_add_u32 s6, s5, s8
	s_nop 0
	v_addc_co_u32_e32 v49, vcc, 0, v97, vcc
	v_add_co_u32_e32 v52, vcc, s21, v96
	global_load_dwordx4 v[48:51], v[48:49], off
	s_nop 0
	v_addc_co_u32_e32 v53, vcc, 0, v97, vcc
	global_load_dwordx4 v[52:55], v[52:53], off
	v_add_co_u32_e32 v56, vcc, s23, v96
	s_addc_u32 s7, s4, 0
	s_nop 0
	v_addc_co_u32_e32 v57, vcc, 0, v97, vcc
	v_add_co_u32_e32 v60, vcc, s25, v96
	global_load_dwordx4 v[56:59], v[56:57], off
	s_nop 0
	v_addc_co_u32_e32 v61, vcc, 0, v97, vcc
	global_load_dwordx4 v[60:63], v[60:61], off
	v_add_co_u32_e32 v64, vcc, s27, v96
	v_readlane_b32 s61, v255, 4
	s_nop 0
	v_addc_co_u32_e32 v65, vcc, 0, v97, vcc
	v_add_co_u32_e32 v68, vcc, s29, v96
	global_load_dwordx4 v[64:67], v[64:65], off
	s_nop 0
	v_addc_co_u32_e32 v69, vcc, 0, v97, vcc
	global_load_dwordx4 v[68:71], v[68:69], off
	v_add_co_u32_e32 v72, vcc, s33, v96
	v_readlane_b32 s62, v255, 5
	s_nop 0
	v_addc_co_u32_e32 v73, vcc, 0, v97, vcc
	v_add_co_u32_e32 v76, vcc, s34, v96
	v_readlane_b32 s63, v255, 6
	s_nop 0
	v_addc_co_u32_e32 v77, vcc, 0, v97, vcc
	global_load_dwordx4 v[72:75], v[72:73], off
	s_nop 0
	global_load_dwordx4 v[76:79], v[76:77], off
	v_add_co_u32_e32 v80, vcc, s35, v96
	v_readlane_b32 s64, v255, 7
	s_nop 0
	v_addc_co_u32_e32 v81, vcc, 0, v97, vcc
	v_add_co_u32_e32 v84, vcc, s38, v96
	v_readlane_b32 s65, v255, 8
	s_nop 0
	v_addc_co_u32_e32 v85, vcc, 0, v97, vcc
	global_load_dwordx4 v[80:83], v[80:81], off
	s_nop 0
	global_load_dwordx4 v[84:87], v[84:85], off
	v_add_co_u32_e32 v88, vcc, s39, v96
	v_readlane_b32 s66, v255, 9
	s_nop 0
	v_addc_co_u32_e32 v89, vcc, 0, v97, vcc
	v_add_co_u32_e32 v92, vcc, s40, v96
	v_readlane_b32 s67, v255, 10
	s_nop 0
	v_addc_co_u32_e32 v93, vcc, 0, v97, vcc
	global_load_dwordx4 v[88:91], v[88:89], off
	s_nop 0
	global_load_dwordx4 v[92:95], v[92:93], off
	v_add_co_u32_e32 v98, vcc, s41, v96
	v_readlane_b32 s68, v255, 11
	s_nop 0
	v_addc_co_u32_e32 v99, vcc, 0, v97, vcc
	v_add_co_u32_e32 v100, vcc, s42, v96
	v_readlane_b32 s69, v255, 12
	s_nop 0
	v_addc_co_u32_e32 v101, vcc, 0, v97, vcc
	global_load_dwordx4 v[96:99], v[98:99], off
	s_nop 0
	global_load_dwordx4 v[100:103], v[100:101], off
	s_waitcnt vmcnt(15)
	v_mul_f32_e32 v4, 0x42800000, v40
	v_mul_f32_e32 v40, 0x42800000, v42
	s_waitcnt vmcnt(14)
	v_mul_f32_e32 v42, 0x42800000, v44
	v_mul_f32_e32 v39, 0x42800000, v41
	ds_write2_b32 v7, v4, v42 offset1:8
	v_mul_f32_e32 v4, 0x42800000, v45
	ds_write2_b32 v7, v39, v4 offset0:129 offset1:137
	v_mul_f32_e32 v4, 0x42800000, v46
	v_mul_f32_e32 v41, 0x42800000, v43
	ds_write2_b32 v37, v40, v4 offset0:2 offset1:10
	v_mul_f32_e32 v4, 0x42800000, v47
	ds_write2_b32 v37, v41, v4 offset0:131 offset1:139
	s_waitcnt vmcnt(13)
	v_mul_f32_e32 v4, 0x42800000, v48
	s_waitcnt vmcnt(12)
	v_mul_f32_e32 v42, 0x42800000, v52
	v_mul_f32_e32 v39, 0x42800000, v49
	ds_write2_b32 v7, v4, v42 offset0:16 offset1:24
	v_mul_f32_e32 v4, 0x42800000, v53
	v_mul_f32_e32 v40, 0x42800000, v50
	ds_write2_b32 v7, v39, v4 offset0:145 offset1:153
	v_mul_f32_e32 v4, 0x42800000, v54
	v_mul_f32_e32 v41, 0x42800000, v51
	ds_write2_b32 v37, v40, v4 offset0:18 offset1:26
	v_mul_f32_e32 v4, 0x42800000, v55
	ds_write2_b32 v37, v41, v4 offset0:147 offset1:155
	s_waitcnt vmcnt(11)
	v_mul_f32_e32 v4, 0x42800000, v56
	s_waitcnt vmcnt(10)
	v_mul_f32_e32 v42, 0x42800000, v60
	v_mul_f32_e32 v39, 0x42800000, v57
	ds_write2_b32 v7, v4, v42 offset0:32 offset1:40
	v_mul_f32_e32 v4, 0x42800000, v61
	v_mul_f32_e32 v40, 0x42800000, v58
	ds_write2_b32 v7, v39, v4 offset0:161 offset1:169
	v_mul_f32_e32 v4, 0x42800000, v62
	v_mul_f32_e32 v41, 0x42800000, v59
	ds_write2_b32 v37, v40, v4 offset0:34 offset1:42
	v_mul_f32_e32 v4, 0x42800000, v63
	ds_write2_b32 v37, v41, v4 offset0:163 offset1:171
	s_waitcnt vmcnt(9)
	v_mul_f32_e32 v4, 0x42800000, v64
	s_waitcnt vmcnt(8)
	v_mul_f32_e32 v42, 0x42800000, v68
	v_mul_f32_e32 v39, 0x42800000, v65
	ds_write2_b32 v7, v4, v42 offset0:48 offset1:56
	v_mul_f32_e32 v4, 0x42800000, v69
	v_mul_f32_e32 v40, 0x42800000, v66
	ds_write2_b32 v7, v39, v4 offset0:177 offset1:185
	v_mul_f32_e32 v4, 0x42800000, v70
	v_mul_f32_e32 v41, 0x42800000, v67
	ds_write2_b32 v37, v40, v4 offset0:50 offset1:58
	v_mul_f32_e32 v4, 0x42800000, v71
	ds_write2_b32 v37, v41, v4 offset0:179 offset1:187
	s_waitcnt vmcnt(7)
	v_mul_f32_e32 v4, 0x42800000, v72
	s_waitcnt vmcnt(6)
	v_mul_f32_e32 v42, 0x42800000, v76
	v_mul_f32_e32 v39, 0x42800000, v73
	ds_write2_b32 v7, v4, v42 offset0:64 offset1:72
	v_mul_f32_e32 v4, 0x42800000, v77
	v_mul_f32_e32 v40, 0x42800000, v74
	ds_write2_b32 v7, v39, v4 offset0:193 offset1:201
	v_mul_f32_e32 v4, 0x42800000, v78
	v_mul_f32_e32 v41, 0x42800000, v75
	ds_write2_b32 v37, v40, v4 offset0:66 offset1:74
	v_mul_f32_e32 v4, 0x42800000, v79
	ds_write2_b32 v37, v41, v4 offset0:195 offset1:203
	s_waitcnt vmcnt(5)
	v_mul_f32_e32 v4, 0x42800000, v80
	s_waitcnt vmcnt(4)
	v_mul_f32_e32 v42, 0x42800000, v84
	v_mul_f32_e32 v39, 0x42800000, v81
	ds_write2_b32 v7, v4, v42 offset0:80 offset1:88
	v_mul_f32_e32 v4, 0x42800000, v85
	v_mul_f32_e32 v40, 0x42800000, v82
	ds_write2_b32 v7, v39, v4 offset0:209 offset1:217
	v_mul_f32_e32 v4, 0x42800000, v86
	v_mul_f32_e32 v41, 0x42800000, v83
	ds_write2_b32 v37, v40, v4 offset0:82 offset1:90
	v_mul_f32_e32 v4, 0x42800000, v87
	ds_write2_b32 v37, v41, v4 offset0:211 offset1:219
	s_waitcnt vmcnt(3)
	v_mul_f32_e32 v4, 0x42800000, v88
	s_waitcnt vmcnt(2)
	v_mul_f32_e32 v42, 0x42800000, v92
	v_mul_f32_e32 v39, 0x42800000, v89
	ds_write2_b32 v7, v4, v42 offset0:96 offset1:104
	v_mul_f32_e32 v4, 0x42800000, v93
	v_mul_f32_e32 v40, 0x42800000, v90
	ds_write2_b32 v7, v39, v4 offset0:225 offset1:233
	v_mul_f32_e32 v4, 0x42800000, v94
	v_mul_f32_e32 v41, 0x42800000, v91
	ds_write2_b32 v37, v40, v4 offset0:98 offset1:106
	v_mul_f32_e32 v4, 0x42800000, v95
	ds_write2_b32 v37, v41, v4 offset0:227 offset1:235
	s_waitcnt vmcnt(1)
	v_mul_f32_e32 v4, 0x42800000, v96
	s_waitcnt vmcnt(0)
	v_mul_f32_e32 v42, 0x42800000, v100
	v_mul_f32_e32 v39, 0x42800000, v97
	ds_write2_b32 v7, v4, v42 offset0:112 offset1:120
	v_mul_f32_e32 v4, 0x42800000, v101
	v_mul_f32_e32 v40, 0x42800000, v98
	ds_write2_b32 v7, v39, v4 offset0:241 offset1:249
	v_mul_f32_e32 v4, 0x42800000, v102
	v_mul_f32_e32 v41, 0x42800000, v99
	ds_write2_b32 v37, v40, v4 offset0:114 offset1:122
	v_mul_f32_e32 v4, 0x42800000, v103
	ds_write2_b32 v37, v41, v4 offset0:243 offset1:251
	s_waitcnt lgkmcnt(0)
	ds_read2_b32 v[40:41], v12 offset1:1
	ds_read2_b32 v[42:43], v12 offset0:2 offset1:3
	ds_read2_b32 v[44:45], v12 offset0:4 offset1:5
	ds_read2_b32 v[46:47], v12 offset0:6 offset1:7
	v_lshl_add_u64 v[48:49], s[6:7], 0, v[2:3]
	v_readlane_b32 s70, v255, 13
	v_readlane_b32 s71, v255, 14
	s_waitcnt lgkmcnt(3)
	v_med3_f32 v4, v40, s31, v38
	v_med3_f32 v39, v41, s31, v38
	v_mov_b32_e32 v40, v5
	v_cvt_pk_fp8_f32 v40, v4, v39
	s_waitcnt lgkmcnt(2)
	v_med3_f32 v4, v42, s31, v38
	v_med3_f32 v39, v43, s31, v38
	v_mov_b32_e32 v41, v5
	v_cvt_pk_fp8_f32 v40, v4, v39 op_sel:[0,0,1]
	s_waitcnt lgkmcnt(1)
	v_med3_f32 v4, v44, s31, v38
	v_med3_f32 v39, v45, s31, v38
	ds_read2_b32 v[42:43], v12 offset0:8 offset1:9
	v_cvt_pk_fp8_f32 v41, v4, v39
	s_waitcnt lgkmcnt(1)
	v_med3_f32 v4, v46, s31, v38
	v_med3_f32 v39, v47, s31, v38
	ds_read2_b32 v[44:45], v12 offset0:10 offset1:11
	ds_read2_b32 v[46:47], v12 offset0:12 offset1:13
	ds_read2_b32 v[50:51], v12 offset0:14 offset1:15
	v_cvt_pk_fp8_f32 v41, v4, v39 op_sel:[0,0,1]
	s_waitcnt lgkmcnt(3)
	v_med3_f32 v4, v42, s31, v38
	v_med3_f32 v39, v43, s31, v38
	v_mov_b32_e32 v42, v5
	v_cvt_pk_fp8_f32 v42, v4, v39
	s_waitcnt lgkmcnt(2)
	v_med3_f32 v4, v44, s31, v38
	v_med3_f32 v39, v45, s31, v38
	s_waitcnt lgkmcnt(1)
	v_med3_f32 v44, v46, s31, v38
	v_med3_f32 v45, v47, s31, v38
	v_mov_b32_e32 v43, v5
	v_cvt_pk_fp8_f32 v43, v44, v45
	ds_read2_b32 v[44:45], v13 offset1:1
	v_cvt_pk_fp8_f32 v42, v4, v39 op_sel:[0,0,1]
	s_waitcnt lgkmcnt(1)
	v_med3_f32 v4, v50, s31, v38
	v_med3_f32 v39, v51, s31, v38
	v_cvt_pk_fp8_f32 v43, v4, v39 op_sel:[0,0,1]
	v_or_b32_e32 v4, s2, v1
	v_lshlrev_b32_e32 v4, 10, v4
	v_lshl_add_u64 v[46:47], v[48:49], 0, v[4:5]
	s_waitcnt lgkmcnt(0)
	v_med3_f32 v4, v44, s31, v38
	v_med3_f32 v39, v45, s31, v38
	v_mov_b32_e32 v44, v5
	ds_read2_b32 v[50:51], v14 offset1:1
	ds_read2_b32 v[52:53], v15 offset1:1
	ds_read2_b32 v[54:55], v16 offset1:1
	v_cvt_pk_fp8_f32 v44, v4, v39
	global_store_dwordx4 v[46:47], v[40:43], off nt
	s_waitcnt lgkmcnt(2)
	v_med3_f32 v4, v50, s31, v38
	v_med3_f32 v39, v51, s31, v38
	v_cvt_pk_fp8_f32 v44, v4, v39 op_sel:[0,0,1]
	s_waitcnt lgkmcnt(1)
	v_med3_f32 v4, v52, s31, v38
	v_med3_f32 v39, v53, s31, v38
	v_mov_b32_e32 v45, v5
	ds_read2_b32 v[40:41], v17 offset1:1
	v_cvt_pk_fp8_f32 v45, v4, v39
	ds_read2_b32 v[42:43], v18 offset1:1
	ds_read2_b32 v[50:51], v19 offset1:1
	ds_read2_b32 v[52:53], v20 offset1:1
	s_waitcnt lgkmcnt(4)
	v_med3_f32 v4, v54, s31, v38
	v_med3_f32 v39, v55, s31, v38
	v_cvt_pk_fp8_f32 v45, v4, v39 op_sel:[0,0,1]
	s_waitcnt lgkmcnt(3)
	v_med3_f32 v4, v40, s31, v38
	v_med3_f32 v39, v41, s31, v38
	v_mov_b32_e32 v46, v5
	v_cvt_pk_fp8_f32 v46, v4, v39
	s_waitcnt lgkmcnt(1)
	v_med3_f32 v40, v50, s31, v38
	v_med3_f32 v41, v51, s31, v38
	v_mov_b32_e32 v47, v5
	v_cvt_pk_fp8_f32 v47, v40, v41
	ds_read2_b32 v[40:41], v21 offset1:1
	v_med3_f32 v4, v42, s31, v38
	v_med3_f32 v39, v43, s31, v38
	v_cvt_pk_fp8_f32 v46, v4, v39 op_sel:[0,0,1]
	s_waitcnt lgkmcnt(1)
	v_med3_f32 v4, v52, s31, v38
	v_med3_f32 v39, v53, s31, v38
	v_cvt_pk_fp8_f32 v47, v4, v39 op_sel:[0,0,1]
	v_or_b32_e32 v4, s2, v8
	v_lshlrev_b32_e32 v4, 10, v4
	v_lshl_add_u64 v[42:43], v[48:49], 0, v[4:5]
	s_waitcnt lgkmcnt(0)
	v_med3_f32 v4, v40, s31, v38
	v_med3_f32 v39, v41, s31, v38
	v_mov_b32_e32 v40, v5
	ds_read2_b32 v[50:51], v22 offset1:1
	ds_read2_b32 v[52:53], v23 offset1:1
	ds_read2_b32 v[54:55], v24 offset1:1
	v_cvt_pk_fp8_f32 v40, v4, v39
	global_store_dwordx4 v[42:43], v[44:47], off nt
	s_waitcnt lgkmcnt(2)
	v_med3_f32 v4, v50, s31, v38
	v_med3_f32 v39, v51, s31, v38
	v_cvt_pk_fp8_f32 v40, v4, v39 op_sel:[0,0,1]
	s_waitcnt lgkmcnt(1)
	v_med3_f32 v4, v52, s31, v38
	v_med3_f32 v39, v53, s31, v38
	v_mov_b32_e32 v41, v5
	ds_read2_b32 v[42:43], v25 offset1:1
	v_cvt_pk_fp8_f32 v41, v4, v39
	ds_read2_b32 v[44:45], v26 offset1:1
	ds_read2_b32 v[46:47], v27 offset1:1
	ds_read2_b32 v[50:51], v28 offset1:1
	s_waitcnt lgkmcnt(4)
	v_med3_f32 v4, v54, s31, v38
	v_med3_f32 v39, v55, s31, v38
	v_cvt_pk_fp8_f32 v41, v4, v39 op_sel:[0,0,1]
	s_waitcnt lgkmcnt(3)
	v_med3_f32 v4, v42, s31, v38
	v_med3_f32 v39, v43, s31, v38
	v_mov_b32_e32 v42, v5
	v_cvt_pk_fp8_f32 v42, v4, v39
	s_waitcnt lgkmcnt(2)
	v_med3_f32 v4, v44, s31, v38
	v_med3_f32 v39, v45, s31, v38
	s_waitcnt lgkmcnt(1)
	v_med3_f32 v44, v46, s31, v38
	v_med3_f32 v45, v47, s31, v38
	v_mov_b32_e32 v43, v5
	v_cvt_pk_fp8_f32 v43, v44, v45
	ds_read2_b32 v[44:45], v29 offset1:1
	v_cvt_pk_fp8_f32 v42, v4, v39 op_sel:[0,0,1]
	s_waitcnt lgkmcnt(1)
	v_med3_f32 v4, v50, s31, v38
	v_med3_f32 v39, v51, s31, v38
	v_cvt_pk_fp8_f32 v43, v4, v39 op_sel:[0,0,1]
	v_or_b32_e32 v4, s2, v9
	v_lshlrev_b32_e32 v4, 10, v4
	v_lshl_add_u64 v[46:47], v[48:49], 0, v[4:5]
	s_waitcnt lgkmcnt(0)
	v_med3_f32 v4, v44, s31, v38
	v_med3_f32 v39, v45, s31, v38
	v_mov_b32_e32 v44, v5
	ds_read2_b32 v[50:51], v30 offset1:1
	ds_read2_b32 v[52:53], v31 offset1:1
	ds_read2_b32 v[54:55], v32 offset1:1
	v_cvt_pk_fp8_f32 v44, v4, v39
	global_store_dwordx4 v[46:47], v[40:43], off nt
	s_waitcnt lgkmcnt(2)
	v_med3_f32 v4, v50, s31, v38
	v_med3_f32 v39, v51, s31, v38
	v_cvt_pk_fp8_f32 v44, v4, v39 op_sel:[0,0,1]
	s_waitcnt lgkmcnt(1)
	v_med3_f32 v4, v52, s31, v38
	v_med3_f32 v39, v53, s31, v38
	v_mov_b32_e32 v45, v5
	ds_read2_b32 v[40:41], v33 offset1:1
	v_cvt_pk_fp8_f32 v45, v4, v39
	ds_read2_b32 v[42:43], v34 offset1:1
	ds_read2_b32 v[50:51], v35 offset1:1
	ds_read2_b32 v[52:53], v36 offset1:1
	s_waitcnt lgkmcnt(4)
	v_med3_f32 v4, v54, s31, v38
	v_med3_f32 v39, v55, s31, v38
	v_cvt_pk_fp8_f32 v45, v4, v39 op_sel:[0,0,1]
	s_waitcnt lgkmcnt(3)
	v_med3_f32 v4, v40, s31, v38
	v_med3_f32 v39, v41, s31, v38
	v_mov_b32_e32 v46, v5
	v_cvt_pk_fp8_f32 v46, v4, v39
	s_waitcnt lgkmcnt(1)
	v_med3_f32 v40, v50, s31, v38
	v_med3_f32 v41, v51, s31, v38
	v_mov_b32_e32 v47, v5
	v_cvt_pk_fp8_f32 v47, v40, v41
	v_med3_f32 v4, v42, s31, v38
	v_med3_f32 v39, v43, s31, v38
	v_cvt_pk_fp8_f32 v46, v4, v39 op_sel:[0,0,1]
	s_waitcnt lgkmcnt(0)
	v_med3_f32 v4, v52, s31, v38
	v_med3_f32 v39, v53, s31, v38
	v_cvt_pk_fp8_f32 v47, v4, v39 op_sel:[0,0,1]
	v_or_b32_e32 v4, s2, v10
	v_lshlrev_b32_e32 v4, 10, v4
	v_lshl_add_u64 v[40:41], v[48:49], 0, v[4:5]
	global_store_dwordx4 v[40:41], v[44:47], off nt
	s_waitcnt lgkmcnt(0)
	s_mov_b64 s[54:55], s[74:75]
	s_branch .LBB0_687
